# baseline (speedup 1.0000x reference)
.Lmy_loopb:
	ds_read_b128 v[158:161], v248 offset:0
	ds_read_b128 v[162:165], v248 offset:1024
	ds_read_b128 v[166:169], v249 offset:2048
	ds_read_b128 v[170:173], v249 offset:3072
	v_mfma_f32_16x16x32_f16 v[218:221], v[82:85], v[150:153], v[106:109]
	v_mfma_f32_16x16x32_f16 v[222:225], v[90:93], v[150:153], v[110:113]
	v_mfma_f32_16x16x32_f16 v[218:221], v[86:89], v[154:157], v[218:221]
	v_mfma_f32_16x16x32_f16 v[222:225], v[94:97], v[154:157], v[222:225]
	s_waitcnt lgkmcnt(2)
	v_mfma_f32_16x16x32_f16 v[210:213], v[54:57], v[158:161], v[210:213]
	v_mfma_f32_16x16x32_f16 v[210:213], v[58:61], v[162:165], v[210:213]
	s_waitcnt lgkmcnt(0)
	v_mfma_f32_16x16x32_f16 v[210:213], v[62:65], v[166:169], v[210:213]
	v_mfma_f32_16x16x32_f16 v[210:213], v[50:53], v[170:173], v[210:213]
	s_waitcnt vmcnt(9)
	v_cvt_pk_f16_f32 v251, v192, v193
	ds_write_b32 v1, v251 offset:0
	ds_read_b128 v[150:153], v186 offset:6144
	ds_read_b128 v[154:157], v186 offset:7168
	s_nop 2
	v_exp_f32_e32 v226, v210
	v_exp_f32_e32 v227, v211
	v_mfma_f32_16x16x32_f16 v[214:217], v[34:37], v[158:161], v[214:217]
	v_min_f32_e32 v228, s42, v212
	v_exp_f32_e32 v229, v213
	v_mfma_f32_16x16x32_f16 v[214:217], v[38:41], v[162:165], v[214:217]
	v_exp_f32_e32 v228, v228
	v_add_f32_e32 v227, 1.0, v227
	v_mfma_f32_16x16x32_f16 v[214:217], v[42:45], v[166:169], v[214:217]
	v_fma_f32 v230, v228, s41, s41
	v_rcp_f32_e32 v227, v227
	v_mfma_f32_16x16x32_f16 v[214:217], v[46:49], v[170:173], v[214:217]
	v_fma_f32 v230, v226, v230, v230
	v_rcp_f32_e32 v230, v230
	v_mfma_f32_16x16x32_f16 v[218:221], v[18:21], v[158:161], v[218:221]
	v_fma_f32 v226, -v228, v230, v230
	v_fma_f32 v200, v200, v227, v226
	v_mfma_f32_16x16x32_f16 v[218:221], v[14:17], v[162:165], v[218:221]
	v_exp_f32_e32 v226, v200
	s_nop 0
	v_add_f32_e32 v227, 1.0, v226
	v_mfma_f32_16x16x32_f16 v[218:221], v[10:13], v[166:169], v[218:221]
	v_fma_f32 v227, v229, v227, v227
	v_rcp_f32_e32 v227, v227
	v_mfma_f32_16x16x32_f16 v[218:221], v[26:29], v[170:173], v[218:221]
	v_fma_f32 v226, -v226, v227, v227
	v_exp_f32_e32 v231, v214
	v_mfma_f32_16x16x32_f16 v[222:225], v[2:5], v[158:161], v[222:225]
	v_exp_f32_e32 v232, v215
	v_min_f32_e32 v233, s42, v216
	v_mfma_f32_16x16x32_f16 v[222:225], v[6:9], v[162:165], v[222:225]
	v_exp_f32_e32 v234, v217
	v_exp_f32_e32 v233, v233
	v_mfma_f32_16x16x32_f16 v[222:225], v[22:25], v[166:169], v[222:225]
	v_exp_f32_e32 v236, v218
	v_add_f32_e32 v232, 1.0, v232
	v_mfma_f32_16x16x32_f16 v[222:225], v[30:33], v[170:173], v[222:225]
	v_fma_f32 v235, v233, s41, s41
	v_exp_f32_e32 v227, v219
	v_rcp_f32_e32 v232, v232
	v_fma_f32 v235, v231, v235, v235
	v_min_f32_e32 v228, s42, v220
	v_rcp_f32_e32 v235, v235
	s_nop 0
	v_fma_f32 v231, -v233, v235, v235
	v_exp_f32_e32 v229, v221
	v_fma_f32 v201, v201, v232, v231
	v_exp_f32_e32 v231, v201
	v_exp_f32_e32 v228, v228
	v_add_f32_e32 v232, 1.0, v231
	v_fma_f32 v232, v234, v232, v232
	v_add_f32_e32 v227, 1.0, v227
	v_rcp_f32_e32 v232, v232
	v_mfma_f32_16x16x32_f16 v[146:149], v[122:125], v[158:161], v[146:149]
	v_fma_f32 v231, -v231, v232, v232
	v_fma_f32 v230, v228, s41, s41
	v_cvt_pk_f16_f32 v246, v226, v231
	v_mfma_f32_16x16x32_f16 v[146:149], v[126:129], v[162:165], v[146:149]
	v_exp_f32_e32 v231, v222
	v_rcp_f32_e32 v227, v227
	v_exp_f32_e32 v232, v223
	buffer_load_dwordx4 v[122:125], v189, s[76:79], s46 offen
	buffer_load_dwordx4 v[126:129], v208, s[76:79], s46 offen
	v_min_f32_e32 v233, s42, v224
	v_fma_f32 v230, v236, v230, v230
	v_exp_f32_e32 v234, v225
	s_waitcnt lgkmcnt(0)
	v_mfma_f32_16x16x32_f16 v[210:213], v[70:73], v[150:153], v[98:101]
	v_exp_f32_e32 v233, v233
	v_rcp_f32_e32 v230, v230
	v_add_f32_e32 v232, 1.0, v232
	v_mfma_f32_16x16x32_f16 v[214:217], v[74:77], v[150:153], v[102:105]
	v_fma_f32 v235, v233, s41, s41
	v_fma_f32 v236, -v228, v230, v230
	v_rcp_f32_e32 v232, v232
	v_fma_f32 v235, v231, v235, v235
	v_fma_f32 v198, v198, v227, v236
	v_rcp_f32_e32 v235, v235
	s_nop 0
	v_fma_f32 v231, -v233, v235, v235
	v_exp_f32_e32 v236, v198
	v_fma_f32 v199, v199, v232, v231
	v_exp_f32_e32 v231, v199
	v_add_f32_e32 v227, 1.0, v236
	v_add_f32_e32 v232, 1.0, v231
	v_fma_f32 v232, v234, v232, v232
	v_fma_f32 v227, v229, v227, v227
	v_rcp_f32_e32 v232, v232
	s_nop 0
	v_fma_f32 v231, -v231, v232, v232
	v_rcp_f32_e32 v227, v227
	s_nop 0
	v_fma_f32 v236, -v236, v227, v227
	v_cvt_pk_f16_f32 v247, v236, v231
	ds_write_b64 v250, v[246:247] offset:12288
	v_mfma_f32_16x16x32_f16 v[210:213], v[66:69], v[154:157], v[210:213]
	v_mfma_f32_16x16x32_f16 v[214:217], v[78:81], v[154:157], v[214:217]
	buffer_load_dwordx2 v[192:193], v209, s[56:59], s45 offen
	s_waitcnt lgkmcnt(0)
	s_barrier
	ds_read_b128 v[158:161], v248 offset:4096
	ds_read_b128 v[162:165], v248 offset:5120
	ds_read_b128 v[166:169], v249 offset:6144
	ds_read_b128 v[170:173], v249 offset:7168
	v_mfma_f32_16x16x32_f16 v[218:221], v[82:85], v[150:153], v[106:109]
	v_mfma_f32_16x16x32_f16 v[222:225], v[90:93], v[150:153], v[110:113]
	v_mfma_f32_16x16x32_f16 v[218:221], v[86:89], v[154:157], v[218:221]
	v_mfma_f32_16x16x32_f16 v[222:225], v[94:97], v[154:157], v[222:225]
	s_waitcnt lgkmcnt(2)
	v_mfma_f32_16x16x32_f16 v[210:213], v[54:57], v[158:161], v[210:213]
	v_mfma_f32_16x16x32_f16 v[210:213], v[58:61], v[162:165], v[210:213]
	s_waitcnt lgkmcnt(0)
	v_mfma_f32_16x16x32_f16 v[210:213], v[62:65], v[166:169], v[210:213]
	v_mfma_f32_16x16x32_f16 v[210:213], v[50:53], v[170:173], v[210:213]
	s_waitcnt vmcnt(9)
	v_cvt_pk_f16_f32 v251, v190, v191
	ds_write_b32 v1, v251 offset:2048
	ds_read_b128 v[150:153], v186 offset:0
	ds_read_b128 v[154:157], v186 offset:1024
	s_nop 2
	v_exp_f32_e32 v226, v210
	v_exp_f32_e32 v227, v211
	v_mfma_f32_16x16x32_f16 v[214:217], v[34:37], v[158:161], v[214:217]
	v_min_f32_e32 v228, s42, v212
	v_exp_f32_e32 v229, v213
	v_mfma_f32_16x16x32_f16 v[214:217], v[38:41], v[162:165], v[214:217]
	v_exp_f32_e32 v228, v228
	v_add_f32_e32 v227, 1.0, v227
	v_mfma_f32_16x16x32_f16 v[214:217], v[42:45], v[166:169], v[214:217]
	v_fma_f32 v230, v228, s41, s41
	v_rcp_f32_e32 v227, v227
	v_mfma_f32_16x16x32_f16 v[214:217], v[46:49], v[170:173], v[214:217]
	v_fma_f32 v230, v226, v230, v230
	v_rcp_f32_e32 v230, v230
	v_mfma_f32_16x16x32_f16 v[218:221], v[18:21], v[158:161], v[218:221]
	v_fma_f32 v226, -v228, v230, v230
	v_fma_f32 v200, v200, v227, v226
	v_mfma_f32_16x16x32_f16 v[218:221], v[14:17], v[162:165], v[218:221]
	v_exp_f32_e32 v226, v200
	s_nop 0
	v_add_f32_e32 v227, 1.0, v226
	v_mfma_f32_16x16x32_f16 v[218:221], v[10:13], v[166:169], v[218:221]
	v_fma_f32 v227, v229, v227, v227
	v_rcp_f32_e32 v227, v227
	v_mfma_f32_16x16x32_f16 v[218:221], v[26:29], v[170:173], v[218:221]
	v_fma_f32 v226, -v226, v227, v227
	v_exp_f32_e32 v231, v214
	v_mfma_f32_16x16x32_f16 v[222:225], v[2:5], v[158:161], v[222:225]
	v_exp_f32_e32 v232, v215
	v_min_f32_e32 v233, s42, v216
	v_mfma_f32_16x16x32_f16 v[222:225], v[6:9], v[162:165], v[222:225]
	v_exp_f32_e32 v234, v217
	v_exp_f32_e32 v233, v233
	v_mfma_f32_16x16x32_f16 v[222:225], v[22:25], v[166:169], v[222:225]
	v_exp_f32_e32 v236, v218
	v_add_f32_e32 v232, 1.0, v232
	v_mfma_f32_16x16x32_f16 v[222:225], v[30:33], v[170:173], v[222:225]
	v_fma_f32 v235, v233, s41, s41
	v_exp_f32_e32 v227, v219
	v_rcp_f32_e32 v232, v232
	v_fma_f32 v235, v231, v235, v235
	v_min_f32_e32 v228, s42, v220
	v_rcp_f32_e32 v235, v235
	s_nop 0
	v_fma_f32 v231, -v233, v235, v235
	v_exp_f32_e32 v229, v221
	v_fma_f32 v201, v201, v232, v231
	v_exp_f32_e32 v231, v201
	v_exp_f32_e32 v228, v228
	v_add_f32_e32 v232, 1.0, v231
	v_fma_f32 v232, v234, v232, v232
	v_add_f32_e32 v227, 1.0, v227
	v_rcp_f32_e32 v232, v232
	v_mfma_f32_16x16x32_f16 v[146:149], v[114:117], v[158:161], v[146:149]
	v_fma_f32 v231, -v231, v232, v232
	v_fma_f32 v230, v228, s41, s41
	v_cvt_pk_f16_f32 v246, v226, v231
	v_mfma_f32_16x16x32_f16 v[146:149], v[118:121], v[162:165], v[146:149]
	v_exp_f32_e32 v231, v222
	v_rcp_f32_e32 v227, v227
	v_exp_f32_e32 v232, v223
	buffer_load_dwordx4 v[114:117], v189, s[80:83], s46 offen
	buffer_load_dwordx4 v[118:121], v208, s[80:83], s46 offen
	v_min_f32_e32 v233, s42, v224
	v_fma_f32 v230, v236, v230, v230
	v_exp_f32_e32 v234, v225
	s_waitcnt lgkmcnt(0)
	v_mfma_f32_16x16x32_f16 v[210:213], v[70:73], v[150:153], v[98:101]
	v_exp_f32_e32 v233, v233
	v_rcp_f32_e32 v230, v230
	v_add_f32_e32 v232, 1.0, v232
	v_mfma_f32_16x16x32_f16 v[214:217], v[74:77], v[150:153], v[102:105]
	v_fma_f32 v235, v233, s41, s41
	v_fma_f32 v236, -v228, v230, v230
	v_rcp_f32_e32 v232, v232
	v_fma_f32 v235, v231, v235, v235
	v_fma_f32 v198, v198, v227, v236
	v_rcp_f32_e32 v235, v235
	s_nop 0
	v_fma_f32 v231, -v233, v235, v235
	v_exp_f32_e32 v236, v198
	v_fma_f32 v199, v199, v232, v231
	v_exp_f32_e32 v231, v199
	v_add_f32_e32 v227, 1.0, v236
	v_add_f32_e32 v232, 1.0, v231
	v_fma_f32 v232, v234, v232, v232
	v_fma_f32 v227, v229, v227, v227
	v_rcp_f32_e32 v232, v232
	s_nop 0
	v_fma_f32 v231, -v231, v232, v232
	v_rcp_f32_e32 v227, v227
	s_nop 0
	v_fma_f32 v236, -v236, v227, v227
	v_cvt_pk_f16_f32 v247, v236, v231
	ds_write_b64 v250, v[246:247] offset:16384
	v_mfma_f32_16x16x32_f16 v[210:213], v[66:69], v[154:157], v[210:213]
	v_mfma_f32_16x16x32_f16 v[214:217], v[78:81], v[154:157], v[214:217]
	buffer_load_dwordx2 v[190:191], v209, s[60:63], s45 offen
	s_add_i32 s45, s45, 0x400000
	s_add_i32 s46, s46, 0x10000
	s_waitcnt lgkmcnt(0)
	s_barrier
	ds_read_b128 v[158:161], v248 offset:8192
	ds_read_b128 v[162:165], v248 offset:9216
	ds_read_b128 v[166:169], v249 offset:10240
	ds_read_b128 v[170:173], v249 offset:11264
	v_mfma_f32_16x16x32_f16 v[218:221], v[82:85], v[150:153], v[106:109]
	v_mfma_f32_16x16x32_f16 v[222:225], v[90:93], v[150:153], v[110:113]
	v_mfma_f32_16x16x32_f16 v[218:221], v[86:89], v[154:157], v[218:221]
	v_mfma_f32_16x16x32_f16 v[222:225], v[94:97], v[154:157], v[222:225]
	s_waitcnt lgkmcnt(2)
	v_mfma_f32_16x16x32_f16 v[210:213], v[54:57], v[158:161], v[210:213]
	v_mfma_f32_16x16x32_f16 v[210:213], v[58:61], v[162:165], v[210:213]
	s_waitcnt lgkmcnt(0)
	v_mfma_f32_16x16x32_f16 v[210:213], v[62:65], v[166:169], v[210:213]
	v_mfma_f32_16x16x32_f16 v[210:213], v[50:53], v[170:173], v[210:213]
	s_waitcnt vmcnt(9)
	v_cvt_pk_f16_f32 v251, v196, v197
	ds_write_b32 v1, v251 offset:4096
	ds_read_b128 v[150:153], v186 offset:2048
	ds_read_b128 v[154:157], v186 offset:3072
	s_nop 2
	v_exp_f32_e32 v226, v210
	v_exp_f32_e32 v227, v211
	v_mfma_f32_16x16x32_f16 v[214:217], v[34:37], v[158:161], v[214:217]
	v_min_f32_e32 v228, s42, v212
	v_exp_f32_e32 v229, v213
	v_mfma_f32_16x16x32_f16 v[214:217], v[38:41], v[162:165], v[214:217]
	v_exp_f32_e32 v228, v228
	v_add_f32_e32 v227, 1.0, v227
	v_mfma_f32_16x16x32_f16 v[214:217], v[42:45], v[166:169], v[214:217]
	v_fma_f32 v230, v228, s41, s41
	v_rcp_f32_e32 v227, v227
	v_mfma_f32_16x16x32_f16 v[214:217], v[46:49], v[170:173], v[214:217]
	v_fma_f32 v230, v226, v230, v230
	v_rcp_f32_e32 v230, v230
	v_mfma_f32_16x16x32_f16 v[218:221], v[18:21], v[158:161], v[218:221]
	v_fma_f32 v226, -v228, v230, v230
	v_fma_f32 v200, v200, v227, v226
	v_mfma_f32_16x16x32_f16 v[218:221], v[14:17], v[162:165], v[218:221]
	v_exp_f32_e32 v226, v200
	s_nop 0
	v_add_f32_e32 v227, 1.0, v226
	v_mfma_f32_16x16x32_f16 v[218:221], v[10:13], v[166:169], v[218:221]
	v_fma_f32 v227, v229, v227, v227
	v_rcp_f32_e32 v227, v227
	v_mfma_f32_16x16x32_f16 v[218:221], v[26:29], v[170:173], v[218:221]
	v_fma_f32 v226, -v226, v227, v227
	v_exp_f32_e32 v231, v214
	v_mfma_f32_16x16x32_f16 v[222:225], v[2:5], v[158:161], v[222:225]
	v_exp_f32_e32 v232, v215
	v_min_f32_e32 v233, s42, v216
	v_mfma_f32_16x16x32_f16 v[222:225], v[6:9], v[162:165], v[222:225]
	v_exp_f32_e32 v234, v217
	v_exp_f32_e32 v233, v233
	v_mfma_f32_16x16x32_f16 v[222:225], v[22:25], v[166:169], v[222:225]
	v_exp_f32_e32 v236, v218
	v_add_f32_e32 v232, 1.0, v232
	v_mfma_f32_16x16x32_f16 v[222:225], v[30:33], v[170:173], v[222:225]
	v_fma_f32 v235, v233, s41, s41
	v_exp_f32_e32 v227, v219
	v_rcp_f32_e32 v232, v232
	v_fma_f32 v235, v231, v235, v235
	v_min_f32_e32 v228, s42, v220
	v_rcp_f32_e32 v235, v235
	s_nop 0
	v_fma_f32 v231, -v233, v235, v235
	v_exp_f32_e32 v229, v221
	v_fma_f32 v201, v201, v232, v231
	v_exp_f32_e32 v231, v201
	v_exp_f32_e32 v228, v228
	v_add_f32_e32 v232, 1.0, v231
	v_fma_f32 v232, v234, v232, v232
	v_add_f32_e32 v227, 1.0, v227
	v_rcp_f32_e32 v232, v232
	v_mfma_f32_16x16x32_f16 v[146:149], v[138:141], v[158:161], v[146:149]
	v_fma_f32 v231, -v231, v232, v232
	v_fma_f32 v230, v228, s41, s41
	v_cvt_pk_f16_f32 v246, v226, v231
	v_mfma_f32_16x16x32_f16 v[146:149], v[142:145], v[162:165], v[146:149]
	v_exp_f32_e32 v231, v222
	v_rcp_f32_e32 v227, v227
	v_exp_f32_e32 v232, v223
	buffer_load_dwordx4 v[138:141], v189, s[68:71], s46 offen
	buffer_load_dwordx4 v[142:145], v208, s[68:71], s46 offen
	v_min_f32_e32 v233, s42, v224
	v_fma_f32 v230, v236, v230, v230
	v_exp_f32_e32 v234, v225
	s_waitcnt lgkmcnt(0)
	v_mfma_f32_16x16x32_f16 v[210:213], v[70:73], v[150:153], v[98:101]
	v_exp_f32_e32 v233, v233
	v_rcp_f32_e32 v230, v230
	v_add_f32_e32 v232, 1.0, v232
	v_mfma_f32_16x16x32_f16 v[214:217], v[74:77], v[150:153], v[102:105]
	v_fma_f32 v235, v233, s41, s41
	v_fma_f32 v236, -v228, v230, v230
	v_rcp_f32_e32 v232, v232
	v_fma_f32 v235, v231, v235, v235
	v_fma_f32 v198, v198, v227, v236
	v_rcp_f32_e32 v235, v235
	s_nop 0
	v_fma_f32 v231, -v233, v235, v235
	v_exp_f32_e32 v236, v198
	v_fma_f32 v199, v199, v232, v231
	v_exp_f32_e32 v231, v199
	v_add_f32_e32 v227, 1.0, v236
	v_add_f32_e32 v232, 1.0, v231
	v_fma_f32 v232, v234, v232, v232
	v_fma_f32 v227, v229, v227, v227
	v_rcp_f32_e32 v232, v232
	s_nop 0
	v_fma_f32 v231, -v231, v232, v232
	v_rcp_f32_e32 v227, v227
	s_nop 0
	v_fma_f32 v236, -v236, v227, v227
	v_cvt_pk_f16_f32 v247, v236, v231
	ds_write_b64 v250, v[246:247] offset:20480
	v_mfma_f32_16x16x32_f16 v[210:213], v[66:69], v[154:157], v[210:213]
	v_mfma_f32_16x16x32_f16 v[214:217], v[78:81], v[154:157], v[214:217]
	buffer_load_dwordx2 v[196:197], v209, s[48:51], s45 offen
	s_waitcnt lgkmcnt(0)
	s_barrier
	ds_read_b128 v[158:161], v248 offset:12288
	ds_read_b128 v[162:165], v248 offset:13312
	ds_read_b128 v[166:169], v249 offset:14336
	ds_read_b128 v[170:173], v249 offset:15360
	v_mfma_f32_16x16x32_f16 v[218:221], v[82:85], v[150:153], v[106:109]
	v_mfma_f32_16x16x32_f16 v[222:225], v[90:93], v[150:153], v[110:113]
	v_mfma_f32_16x16x32_f16 v[218:221], v[86:89], v[154:157], v[218:221]
	v_mfma_f32_16x16x32_f16 v[222:225], v[94:97], v[154:157], v[222:225]
	s_waitcnt lgkmcnt(2)
	v_mfma_f32_16x16x32_f16 v[210:213], v[54:57], v[158:161], v[210:213]
	v_mfma_f32_16x16x32_f16 v[210:213], v[58:61], v[162:165], v[210:213]
	s_waitcnt lgkmcnt(0)
	v_mfma_f32_16x16x32_f16 v[210:213], v[62:65], v[166:169], v[210:213]
	v_mfma_f32_16x16x32_f16 v[210:213], v[50:53], v[170:173], v[210:213]
	s_waitcnt vmcnt(9)
	v_cvt_pk_f16_f32 v251, v194, v195
	ds_write_b32 v1, v251 offset:6144
	ds_read_b128 v[150:153], v186 offset:4096
	ds_read_b128 v[154:157], v186 offset:5120
	s_nop 2
	v_exp_f32_e32 v226, v210
	v_exp_f32_e32 v227, v211
	v_mfma_f32_16x16x32_f16 v[214:217], v[34:37], v[158:161], v[214:217]
	v_min_f32_e32 v228, s42, v212
	v_exp_f32_e32 v229, v213
	v_mfma_f32_16x16x32_f16 v[214:217], v[38:41], v[162:165], v[214:217]
	v_exp_f32_e32 v228, v228
	v_add_f32_e32 v227, 1.0, v227
	v_mfma_f32_16x16x32_f16 v[214:217], v[42:45], v[166:169], v[214:217]
	v_fma_f32 v230, v228, s41, s41
	v_rcp_f32_e32 v227, v227
	v_mfma_f32_16x16x32_f16 v[214:217], v[46:49], v[170:173], v[214:217]
	v_fma_f32 v230, v226, v230, v230
	v_rcp_f32_e32 v230, v230
	v_mfma_f32_16x16x32_f16 v[218:221], v[18:21], v[158:161], v[218:221]
	v_fma_f32 v226, -v228, v230, v230
	v_fma_f32 v200, v200, v227, v226
	v_mfma_f32_16x16x32_f16 v[218:221], v[14:17], v[162:165], v[218:221]
	v_exp_f32_e32 v226, v200
	s_nop 0
	v_add_f32_e32 v227, 1.0, v226
	v_mfma_f32_16x16x32_f16 v[218:221], v[10:13], v[166:169], v[218:221]
	v_fma_f32 v227, v229, v227, v227
	v_rcp_f32_e32 v227, v227
	v_mfma_f32_16x16x32_f16 v[218:221], v[26:29], v[170:173], v[218:221]
	v_fma_f32 v226, -v226, v227, v227
	v_exp_f32_e32 v231, v214
	v_mfma_f32_16x16x32_f16 v[222:225], v[2:5], v[158:161], v[222:225]
	v_exp_f32_e32 v232, v215
	v_min_f32_e32 v233, s42, v216
	v_mfma_f32_16x16x32_f16 v[222:225], v[6:9], v[162:165], v[222:225]
	v_exp_f32_e32 v234, v217
	v_exp_f32_e32 v233, v233
	v_mfma_f32_16x16x32_f16 v[222:225], v[22:25], v[166:169], v[222:225]
	v_exp_f32_e32 v236, v218
	v_add_f32_e32 v232, 1.0, v232
	v_mfma_f32_16x16x32_f16 v[222:225], v[30:33], v[170:173], v[222:225]
	v_fma_f32 v235, v233, s41, s41
	v_exp_f32_e32 v227, v219
	v_rcp_f32_e32 v232, v232
	v_fma_f32 v235, v231, v235, v235
	v_min_f32_e32 v228, s42, v220
	v_rcp_f32_e32 v235, v235
	s_nop 0
	v_fma_f32 v231, -v233, v235, v235
	v_exp_f32_e32 v229, v221
	v_fma_f32 v201, v201, v232, v231
	v_exp_f32_e32 v231, v201
	v_exp_f32_e32 v228, v228
	v_add_f32_e32 v232, 1.0, v231
	v_fma_f32 v232, v234, v232, v232
	v_add_f32_e32 v227, 1.0, v227
	v_rcp_f32_e32 v232, v232
	v_mfma_f32_16x16x32_f16 v[146:149], v[130:133], v[158:161], v[146:149]
	v_fma_f32 v231, -v231, v232, v232
	v_fma_f32 v230, v228, s41, s41
	v_cvt_pk_f16_f32 v246, v226, v231
	v_mfma_f32_16x16x32_f16 v[146:149], v[134:137], v[162:165], v[146:149]
	v_exp_f32_e32 v231, v222
	v_rcp_f32_e32 v227, v227
	v_exp_f32_e32 v232, v223
	buffer_load_dwordx4 v[130:133], v189, s[72:75], s46 offen
	buffer_load_dwordx4 v[134:137], v208, s[72:75], s46 offen
	v_min_f32_e32 v233, s42, v224
	v_fma_f32 v230, v236, v230, v230
	v_exp_f32_e32 v234, v225
	s_waitcnt lgkmcnt(0)
	v_mfma_f32_16x16x32_f16 v[210:213], v[70:73], v[150:153], v[98:101]
	v_exp_f32_e32 v233, v233
	v_rcp_f32_e32 v230, v230
	v_add_f32_e32 v232, 1.0, v232
	v_mfma_f32_16x16x32_f16 v[214:217], v[74:77], v[150:153], v[102:105]
	v_fma_f32 v235, v233, s41, s41
	v_fma_f32 v236, -v228, v230, v230
	v_rcp_f32_e32 v232, v232
	v_fma_f32 v235, v231, v235, v235
	v_fma_f32 v198, v198, v227, v236
	v_rcp_f32_e32 v235, v235
	s_nop 0
	v_fma_f32 v231, -v233, v235, v235
	v_exp_f32_e32 v236, v198
	v_fma_f32 v199, v199, v232, v231
	v_exp_f32_e32 v231, v199
	v_add_f32_e32 v227, 1.0, v236
	v_add_f32_e32 v232, 1.0, v231
	v_fma_f32 v232, v234, v232, v232
	v_fma_f32 v227, v229, v227, v227
	v_rcp_f32_e32 v232, v232
	s_nop 0
	v_fma_f32 v231, -v231, v232, v232
	v_rcp_f32_e32 v227, v227
	s_nop 0
	v_fma_f32 v236, -v236, v227, v227
	v_cvt_pk_f16_f32 v247, v236, v231
	ds_write_b64 v250, v[246:247] offset:24576
	v_mfma_f32_16x16x32_f16 v[210:213], v[66:69], v[154:157], v[210:213]
	v_mfma_f32_16x16x32_f16 v[214:217], v[78:81], v[154:157], v[214:217]
	buffer_load_dwordx2 v[194:195], v209, s[52:55], s45 offen
	v_add_u32_e32 v250, 0x4000, v250
	v_add_u32_e32 v248, 0x4000, v248
	v_add_u32_e32 v249, 0x4000, v249
	s_waitcnt lgkmcnt(0)
	s_barrier
	s_cmp_lt_u32 s46, 0xa0000
	s_cbranch_scc1 .Lmy_loopb
	ds_read_b128 v[158:161], v248 offset:0
	ds_read_b128 v[162:165], v248 offset:1024
	ds_read_b128 v[166:169], v249 offset:2048
	ds_read_b128 v[170:173], v249 offset:3072
	v_mfma_f32_16x16x32_f16 v[218:221], v[82:85], v[150:153], v[106:109]
	v_mfma_f32_16x16x32_f16 v[222:225], v[90:93], v[150:153], v[110:113]
	v_mfma_f32_16x16x32_f16 v[218:221], v[86:89], v[154:157], v[218:221]
	v_mfma_f32_16x16x32_f16 v[222:225], v[94:97], v[154:157], v[222:225]
	s_waitcnt lgkmcnt(2)
	v_mfma_f32_16x16x32_f16 v[210:213], v[54:57], v[158:161], v[210:213]
	v_mfma_f32_16x16x32_f16 v[210:213], v[58:61], v[162:165], v[210:213]
	s_waitcnt lgkmcnt(0)
	v_mfma_f32_16x16x32_f16 v[210:213], v[62:65], v[166:169], v[210:213]
	v_mfma_f32_16x16x32_f16 v[210:213], v[50:53], v[170:173], v[210:213]
	s_waitcnt vmcnt(9)
	v_cvt_pk_f16_f32 v251, v192, v193
	ds_write_b32 v1, v251 offset:0
	ds_read_b128 v[150:153], v186 offset:6144
	ds_read_b128 v[154:157], v186 offset:7168
	s_nop 2
	v_exp_f32_e32 v226, v210
	v_exp_f32_e32 v227, v211
	v_mfma_f32_16x16x32_f16 v[214:217], v[34:37], v[158:161], v[214:217]
	v_min_f32_e32 v228, s42, v212
	v_exp_f32_e32 v229, v213
	v_mfma_f32_16x16x32_f16 v[214:217], v[38:41], v[162:165], v[214:217]
	v_exp_f32_e32 v228, v228
	v_add_f32_e32 v227, 1.0, v227
	v_mfma_f32_16x16x32_f16 v[214:217], v[42:45], v[166:169], v[214:217]
	v_fma_f32 v230, v228, s41, s41
	v_rcp_f32_e32 v227, v227
	v_mfma_f32_16x16x32_f16 v[214:217], v[46:49], v[170:173], v[214:217]
	v_fma_f32 v230, v226, v230, v230
	v_rcp_f32_e32 v230, v230
	v_mfma_f32_16x16x32_f16 v[218:221], v[18:21], v[158:161], v[218:221]
	v_fma_f32 v226, -v228, v230, v230
	v_fma_f32 v200, v200, v227, v226
	v_mfma_f32_16x16x32_f16 v[218:221], v[14:17], v[162:165], v[218:221]
	v_min_f32_e32 v226, s42, v200
	v_exp_f32_e32 v226, v226
	v_mfma_f32_16x16x32_f16 v[218:221], v[10:13], v[166:169], v[218:221]
	v_add_f32_e32 v227, 1.0, v226
	v_fma_f32 v227, v229, v227, v227
	v_mfma_f32_16x16x32_f16 v[218:221], v[26:29], v[170:173], v[218:221]
	v_rcp_f32_e32 v227, v227
	v_exp_f32_e32 v231, v214
	v_mfma_f32_16x16x32_f16 v[222:225], v[2:5], v[158:161], v[222:225]
	v_exp_f32_e32 v232, v215
	v_fma_f32 v226, -v226, v227, v227
	v_mfma_f32_16x16x32_f16 v[222:225], v[6:9], v[162:165], v[222:225]
	v_min_f32_e32 v233, s42, v216
	v_exp_f32_e32 v234, v217
	v_mfma_f32_16x16x32_f16 v[222:225], v[22:25], v[166:169], v[222:225]
	v_exp_f32_e32 v236, v218
	v_exp_f32_e32 v233, v233
	v_mfma_f32_16x16x32_f16 v[222:225], v[30:33], v[170:173], v[222:225]
	v_add_f32_e32 v232, 1.0, v232
	v_exp_f32_e32 v227, v219
	v_fma_f32 v235, v233, s41, s41
	v_rcp_f32_e32 v232, v232
	v_min_f32_e32 v228, s42, v220
	v_fma_f32 v235, v231, v235, v235
	v_rcp_f32_e32 v235, v235
	v_exp_f32_e32 v229, v221
	v_fma_f32 v231, -v233, v235, v235
	v_fma_f32 v201, v201, v232, v231
	v_exp_f32_e32 v228, v228
	v_min_f32_e32 v231, s42, v201
	v_exp_f32_e32 v231, v231
	v_add_f32_e32 v227, 1.0, v227
	v_add_f32_e32 v232, 1.0, v231
	v_mfma_f32_16x16x32_f16 v[146:149], v[122:125], v[158:161], v[146:149]
	v_fma_f32 v232, v234, v232, v232
	v_fma_f32 v230, v228, s41, s41
	v_rcp_f32_e32 v232, v232
	v_mfma_f32_16x16x32_f16 v[146:149], v[126:129], v[162:165], v[146:149]
	v_fma_f32 v231, -v231, v232, v232
	v_rcp_f32_e32 v227, v227
	v_cvt_pk_f16_f32 v246, v226, v231
	buffer_load_dwordx4 v[122:125], v189, s[76:79], s46 offen
	buffer_load_dwordx4 v[126:129], v208, s[76:79], s46 offen
	v_exp_f32_e32 v231, v222
	v_fma_f32 v230, v236, v230, v230
	v_exp_f32_e32 v232, v223
	s_waitcnt lgkmcnt(0)
	v_mfma_f32_16x16x32_f16 v[210:213], v[70:73], v[150:153], v[98:101]
	v_min_f32_e32 v233, s42, v224
	v_rcp_f32_e32 v230, v230
	v_exp_f32_e32 v234, v225
	v_mfma_f32_16x16x32_f16 v[214:217], v[74:77], v[150:153], v[102:105]
	v_exp_f32_e32 v233, v233
	v_fma_f32 v236, -v228, v230, v230
	v_add_f32_e32 v232, 1.0, v232
	v_fma_f32 v235, v233, s41, s41
	v_fma_f32 v198, v198, v227, v236
	v_rcp_f32_e32 v232, v232
	v_fma_f32 v235, v231, v235, v235
	v_min_f32_e32 v236, s42, v198
	v_rcp_f32_e32 v235, v235
	s_nop 0
	v_fma_f32 v231, -v233, v235, v235
	v_exp_f32_e32 v236, v236
	v_fma_f32 v199, v199, v232, v231
	v_min_f32_e32 v231, s42, v199
	v_add_f32_e32 v227, 1.0, v236
	v_exp_f32_e32 v231, v231
	v_fma_f32 v227, v229, v227, v227
	v_add_f32_e32 v232, 1.0, v231
	v_rcp_f32_e32 v227, v227
	v_fma_f32 v232, v234, v232, v232
	v_fma_f32 v236, -v236, v227, v227
	v_rcp_f32_e32 v232, v232
	s_nop 0
	v_fma_f32 v231, -v231, v232, v232
	v_cvt_pk_f16_f32 v247, v236, v231
	ds_write_b64 v250, v[246:247] offset:12288
	v_mfma_f32_16x16x32_f16 v[210:213], v[66:69], v[154:157], v[210:213]
	v_mfma_f32_16x16x32_f16 v[214:217], v[78:81], v[154:157], v[214:217]
	buffer_load_dwordx2 v[192:193], v209, s[56:59], s45 offen
	s_waitcnt lgkmcnt(0)
	s_barrier
	ds_read_b128 v[158:161], v248 offset:4096
	ds_read_b128 v[162:165], v248 offset:5120
	ds_read_b128 v[166:169], v249 offset:6144
	ds_read_b128 v[170:173], v249 offset:7168
	v_mfma_f32_16x16x32_f16 v[218:221], v[82:85], v[150:153], v[106:109]
	v_mfma_f32_16x16x32_f16 v[222:225], v[90:93], v[150:153], v[110:113]
	v_mfma_f32_16x16x32_f16 v[218:221], v[86:89], v[154:157], v[218:221]
	v_mfma_f32_16x16x32_f16 v[222:225], v[94:97], v[154:157], v[222:225]
	s_waitcnt lgkmcnt(2)
	v_mfma_f32_16x16x32_f16 v[210:213], v[54:57], v[158:161], v[210:213]
	v_mfma_f32_16x16x32_f16 v[210:213], v[58:61], v[162:165], v[210:213]
	s_waitcnt lgkmcnt(0)
	v_mfma_f32_16x16x32_f16 v[210:213], v[62:65], v[166:169], v[210:213]
	v_mfma_f32_16x16x32_f16 v[210:213], v[50:53], v[170:173], v[210:213]
	s_waitcnt vmcnt(9)
	v_cvt_pk_f16_f32 v251, v190, v191
	ds_write_b32 v1, v251 offset:2048
	ds_read_b128 v[150:153], v186 offset:0
	ds_read_b128 v[154:157], v186 offset:1024
	s_nop 2
	v_exp_f32_e32 v226, v210
	v_exp_f32_e32 v227, v211
	v_mfma_f32_16x16x32_f16 v[214:217], v[34:37], v[158:161], v[214:217]
	v_min_f32_e32 v228, s42, v212
	v_exp_f32_e32 v229, v213
	v_mfma_f32_16x16x32_f16 v[214:217], v[38:41], v[162:165], v[214:217]
	v_exp_f32_e32 v228, v228
	v_add_f32_e32 v227, 1.0, v227
	v_mfma_f32_16x16x32_f16 v[214:217], v[42:45], v[166:169], v[214:217]
	v_fma_f32 v230, v228, s41, s41
	v_rcp_f32_e32 v227, v227
	v_mfma_f32_16x16x32_f16 v[214:217], v[46:49], v[170:173], v[214:217]
	v_fma_f32 v230, v226, v230, v230
	v_rcp_f32_e32 v230, v230
	v_mfma_f32_16x16x32_f16 v[218:221], v[18:21], v[158:161], v[218:221]
	v_fma_f32 v226, -v228, v230, v230
	v_fma_f32 v200, v200, v227, v226
	v_mfma_f32_16x16x32_f16 v[218:221], v[14:17], v[162:165], v[218:221]
	v_min_f32_e32 v226, s42, v200
	v_exp_f32_e32 v226, v226
	v_mfma_f32_16x16x32_f16 v[218:221], v[10:13], v[166:169], v[218:221]
	v_add_f32_e32 v227, 1.0, v226
	v_fma_f32 v227, v229, v227, v227
	v_mfma_f32_16x16x32_f16 v[218:221], v[26:29], v[170:173], v[218:221]
	v_rcp_f32_e32 v227, v227
	v_exp_f32_e32 v231, v214
	v_mfma_f32_16x16x32_f16 v[222:225], v[2:5], v[158:161], v[222:225]
	v_exp_f32_e32 v232, v215
	v_fma_f32 v226, -v226, v227, v227
	v_mfma_f32_16x16x32_f16 v[222:225], v[6:9], v[162:165], v[222:225]
	v_min_f32_e32 v233, s42, v216
	v_exp_f32_e32 v234, v217
	v_mfma_f32_16x16x32_f16 v[222:225], v[22:25], v[166:169], v[222:225]
	v_exp_f32_e32 v236, v218
	v_exp_f32_e32 v233, v233
	v_mfma_f32_16x16x32_f16 v[222:225], v[30:33], v[170:173], v[222:225]
	v_add_f32_e32 v232, 1.0, v232
	v_exp_f32_e32 v227, v219
	v_fma_f32 v235, v233, s41, s41
	v_rcp_f32_e32 v232, v232
	v_min_f32_e32 v228, s42, v220
	v_fma_f32 v235, v231, v235, v235
	v_rcp_f32_e32 v235, v235
	v_exp_f32_e32 v229, v221
	v_fma_f32 v231, -v233, v235, v235
	v_fma_f32 v201, v201, v232, v231
	v_exp_f32_e32 v228, v228
	v_min_f32_e32 v231, s42, v201
	v_exp_f32_e32 v231, v231
	v_add_f32_e32 v227, 1.0, v227
	v_add_f32_e32 v232, 1.0, v231
	v_mfma_f32_16x16x32_f16 v[146:149], v[114:117], v[158:161], v[146:149]
	v_fma_f32 v232, v234, v232, v232
	v_fma_f32 v230, v228, s41, s41
	v_rcp_f32_e32 v232, v232
	v_mfma_f32_16x16x32_f16 v[146:149], v[118:121], v[162:165], v[146:149]
	v_fma_f32 v231, -v231, v232, v232
	v_rcp_f32_e32 v227, v227
	v_cvt_pk_f16_f32 v246, v226, v231
	buffer_load_dwordx4 v[114:117], v189, s[80:83], s46 offen
	buffer_load_dwordx4 v[118:121], v208, s[80:83], s46 offen
	v_exp_f32_e32 v231, v222
	v_fma_f32 v230, v236, v230, v230
	v_exp_f32_e32 v232, v223
	s_waitcnt lgkmcnt(0)
	v_mfma_f32_16x16x32_f16 v[210:213], v[70:73], v[150:153], v[98:101]
	v_min_f32_e32 v233, s42, v224
	v_rcp_f32_e32 v230, v230
	v_exp_f32_e32 v234, v225
	v_mfma_f32_16x16x32_f16 v[214:217], v[74:77], v[150:153], v[102:105]
	v_exp_f32_e32 v233, v233
	v_fma_f32 v236, -v228, v230, v230
	v_add_f32_e32 v232, 1.0, v232
	v_fma_f32 v235, v233, s41, s41
	v_fma_f32 v198, v198, v227, v236
	v_rcp_f32_e32 v232, v232
	v_fma_f32 v235, v231, v235, v235
	v_min_f32_e32 v236, s42, v198
	v_rcp_f32_e32 v235, v235
	s_nop 0
	v_fma_f32 v231, -v233, v235, v235
	v_exp_f32_e32 v236, v236
	v_fma_f32 v199, v199, v232, v231
	v_min_f32_e32 v231, s42, v199
	v_add_f32_e32 v227, 1.0, v236
	v_exp_f32_e32 v231, v231
	v_fma_f32 v227, v229, v227, v227
	v_add_f32_e32 v232, 1.0, v231
	v_rcp_f32_e32 v227, v227
	v_fma_f32 v232, v234, v232, v232
	v_fma_f32 v236, -v236, v227, v227
	v_rcp_f32_e32 v232, v232
	s_nop 0
	v_fma_f32 v231, -v231, v232, v232
	v_cvt_pk_f16_f32 v247, v236, v231
	ds_write_b64 v250, v[246:247] offset:16384
	v_mfma_f32_16x16x32_f16 v[210:213], v[66:69], v[154:157], v[210:213]
	v_mfma_f32_16x16x32_f16 v[214:217], v[78:81], v[154:157], v[214:217]
	buffer_load_dwordx2 v[190:191], v209, s[60:63], s45 offen
	s_add_i32 s45, s45, 0x400000
	s_add_i32 s46, s46, 0x10000
	s_waitcnt lgkmcnt(0)
	s_barrier
	ds_read_b128 v[158:161], v248 offset:8192
	ds_read_b128 v[162:165], v248 offset:9216
	ds_read_b128 v[166:169], v249 offset:10240
	ds_read_b128 v[170:173], v249 offset:11264
	v_mfma_f32_16x16x32_f16 v[218:221], v[82:85], v[150:153], v[106:109]
	v_mfma_f32_16x16x32_f16 v[222:225], v[90:93], v[150:153], v[110:113]
	v_mfma_f32_16x16x32_f16 v[218:221], v[86:89], v[154:157], v[218:221]
	v_mfma_f32_16x16x32_f16 v[222:225], v[94:97], v[154:157], v[222:225]
	s_waitcnt lgkmcnt(2)
	v_mfma_f32_16x16x32_f16 v[210:213], v[54:57], v[158:161], v[210:213]
	v_mfma_f32_16x16x32_f16 v[210:213], v[58:61], v[162:165], v[210:213]
	s_waitcnt lgkmcnt(0)
	v_mfma_f32_16x16x32_f16 v[210:213], v[62:65], v[166:169], v[210:213]
	v_mfma_f32_16x16x32_f16 v[210:213], v[50:53], v[170:173], v[210:213]
	s_waitcnt vmcnt(9)
	v_cvt_pk_f16_f32 v251, v196, v197
	ds_write_b32 v1, v251 offset:4096
	ds_read_b128 v[150:153], v186 offset:2048
	ds_read_b128 v[154:157], v186 offset:3072
	s_nop 2
	v_exp_f32_e32 v226, v210
	v_exp_f32_e32 v227, v211
	v_mfma_f32_16x16x32_f16 v[214:217], v[34:37], v[158:161], v[214:217]
	v_min_f32_e32 v228, s42, v212
	v_exp_f32_e32 v229, v213
	v_mfma_f32_16x16x32_f16 v[214:217], v[38:41], v[162:165], v[214:217]
	v_exp_f32_e32 v228, v228
	v_add_f32_e32 v227, 1.0, v227
	v_mfma_f32_16x16x32_f16 v[214:217], v[42:45], v[166:169], v[214:217]
	v_fma_f32 v230, v228, s41, s41
	v_rcp_f32_e32 v227, v227
	v_mfma_f32_16x16x32_f16 v[214:217], v[46:49], v[170:173], v[214:217]
	v_fma_f32 v230, v226, v230, v230
	v_rcp_f32_e32 v230, v230
	v_mfma_f32_16x16x32_f16 v[218:221], v[18:21], v[158:161], v[218:221]
	v_fma_f32 v226, -v228, v230, v230
	v_fma_f32 v200, v200, v227, v226
	v_mfma_f32_16x16x32_f16 v[218:221], v[14:17], v[162:165], v[218:221]
	v_min_f32_e32 v226, s42, v200
	v_exp_f32_e32 v226, v226
	v_mfma_f32_16x16x32_f16 v[218:221], v[10:13], v[166:169], v[218:221]
	v_add_f32_e32 v227, 1.0, v226
	v_fma_f32 v227, v229, v227, v227
	v_mfma_f32_16x16x32_f16 v[218:221], v[26:29], v[170:173], v[218:221]
	v_rcp_f32_e32 v227, v227
	v_exp_f32_e32 v231, v214
	v_mfma_f32_16x16x32_f16 v[222:225], v[2:5], v[158:161], v[222:225]
	v_exp_f32_e32 v232, v215
	v_fma_f32 v226, -v226, v227, v227
	v_mfma_f32_16x16x32_f16 v[222:225], v[6:9], v[162:165], v[222:225]
	v_min_f32_e32 v233, s42, v216
	v_exp_f32_e32 v234, v217
	v_mfma_f32_16x16x32_f16 v[222:225], v[22:25], v[166:169], v[222:225]
	v_exp_f32_e32 v236, v218
	v_exp_f32_e32 v233, v233
	v_mfma_f32_16x16x32_f16 v[222:225], v[30:33], v[170:173], v[222:225]
	v_add_f32_e32 v232, 1.0, v232
	v_exp_f32_e32 v227, v219
	v_fma_f32 v235, v233, s41, s41
	v_rcp_f32_e32 v232, v232
	v_min_f32_e32 v228, s42, v220
	v_fma_f32 v235, v231, v235, v235
	v_rcp_f32_e32 v235, v235
	v_exp_f32_e32 v229, v221
	v_fma_f32 v231, -v233, v235, v235
	v_fma_f32 v201, v201, v232, v231
	v_exp_f32_e32 v228, v228
	v_min_f32_e32 v231, s42, v201
	v_exp_f32_e32 v231, v231
	v_add_f32_e32 v227, 1.0, v227
	v_add_f32_e32 v232, 1.0, v231
	v_mfma_f32_16x16x32_f16 v[146:149], v[138:141], v[158:161], v[146:149]
	v_fma_f32 v232, v234, v232, v232
	v_fma_f32 v230, v228, s41, s41
	v_rcp_f32_e32 v232, v232
	v_mfma_f32_16x16x32_f16 v[146:149], v[142:145], v[162:165], v[146:149]
	v_fma_f32 v231, -v231, v232, v232
	v_rcp_f32_e32 v227, v227
	v_cvt_pk_f16_f32 v246, v226, v231
	buffer_load_dwordx4 v[138:141], v189, s[68:71], s46 offen
	buffer_load_dwordx4 v[142:145], v208, s[68:71], s46 offen
	v_exp_f32_e32 v231, v222
	v_fma_f32 v230, v236, v230, v230
	v_exp_f32_e32 v232, v223
	s_waitcnt lgkmcnt(0)
	v_mfma_f32_16x16x32_f16 v[210:213], v[70:73], v[150:153], v[98:101]
	v_min_f32_e32 v233, s42, v224
	v_rcp_f32_e32 v230, v230
	v_exp_f32_e32 v234, v225
	v_mfma_f32_16x16x32_f16 v[214:217], v[74:77], v[150:153], v[102:105]
	v_exp_f32_e32 v233, v233
	v_fma_f32 v236, -v228, v230, v230
	v_add_f32_e32 v232, 1.0, v232
	v_fma_f32 v235, v233, s41, s41
	v_fma_f32 v198, v198, v227, v236
	v_rcp_f32_e32 v232, v232
	v_fma_f32 v235, v231, v235, v235
	v_min_f32_e32 v236, s42, v198
	v_rcp_f32_e32 v235, v235
	s_nop 0
	v_fma_f32 v231, -v233, v235, v235
	v_exp_f32_e32 v236, v236
	v_fma_f32 v199, v199, v232, v231
	v_min_f32_e32 v231, s42, v199
	v_add_f32_e32 v227, 1.0, v236
	v_exp_f32_e32 v231, v231
	v_fma_f32 v227, v229, v227, v227
	v_add_f32_e32 v232, 1.0, v231
	v_rcp_f32_e32 v227, v227
	v_fma_f32 v232, v234, v232, v232
	v_fma_f32 v236, -v236, v227, v227
	v_rcp_f32_e32 v232, v232
	s_nop 0
	v_fma_f32 v231, -v231, v232, v232
	v_cvt_pk_f16_f32 v247, v236, v231
	ds_write_b64 v250, v[246:247] offset:20480
	v_mfma_f32_16x16x32_f16 v[210:213], v[66:69], v[154:157], v[210:213]
	v_mfma_f32_16x16x32_f16 v[214:217], v[78:81], v[154:157], v[214:217]
	s_waitcnt lgkmcnt(0)
	s_barrier
	ds_read_b128 v[158:161], v248 offset:12288
	ds_read_b128 v[162:165], v248 offset:13312
	ds_read_b128 v[166:169], v249 offset:14336
	ds_read_b128 v[170:173], v249 offset:15360
	v_mfma_f32_16x16x32_f16 v[218:221], v[82:85], v[150:153], v[106:109]
	v_mfma_f32_16x16x32_f16 v[222:225], v[90:93], v[150:153], v[110:113]
	v_mfma_f32_16x16x32_f16 v[218:221], v[86:89], v[154:157], v[218:221]
	v_mfma_f32_16x16x32_f16 v[222:225], v[94:97], v[154:157], v[222:225]
	s_waitcnt lgkmcnt(2)
	v_mfma_f32_16x16x32_f16 v[210:213], v[54:57], v[158:161], v[210:213]
	v_mfma_f32_16x16x32_f16 v[210:213], v[58:61], v[162:165], v[210:213]
	s_waitcnt lgkmcnt(0)
	v_mfma_f32_16x16x32_f16 v[210:213], v[62:65], v[166:169], v[210:213]
	v_mfma_f32_16x16x32_f16 v[210:213], v[50:53], v[170:173], v[210:213]
	s_waitcnt vmcnt(8)
	v_cvt_pk_f16_f32 v251, v194, v195
	ds_write_b32 v1, v251 offset:6144
	ds_read_b128 v[150:153], v186 offset:4096
	ds_read_b128 v[154:157], v186 offset:5120
	s_nop 2
	v_exp_f32_e32 v226, v210
	v_exp_f32_e32 v227, v211
	v_mfma_f32_16x16x32_f16 v[214:217], v[34:37], v[158:161], v[214:217]
	v_min_f32_e32 v228, s42, v212
	v_exp_f32_e32 v229, v213
	v_mfma_f32_16x16x32_f16 v[214:217], v[38:41], v[162:165], v[214:217]
	v_exp_f32_e32 v228, v228
	v_add_f32_e32 v227, 1.0, v227
	v_mfma_f32_16x16x32_f16 v[214:217], v[42:45], v[166:169], v[214:217]
	v_fma_f32 v230, v228, s41, s41
	v_rcp_f32_e32 v227, v227
	v_mfma_f32_16x16x32_f16 v[214:217], v[46:49], v[170:173], v[214:217]
	v_fma_f32 v230, v226, v230, v230
	v_rcp_f32_e32 v230, v230
	v_mfma_f32_16x16x32_f16 v[218:221], v[18:21], v[158:161], v[218:221]
	v_fma_f32 v226, -v228, v230, v230
	v_fma_f32 v200, v200, v227, v226
	v_mfma_f32_16x16x32_f16 v[218:221], v[14:17], v[162:165], v[218:221]
	v_min_f32_e32 v226, s42, v200
	v_exp_f32_e32 v226, v226
	v_mfma_f32_16x16x32_f16 v[218:221], v[10:13], v[166:169], v[218:221]
	v_add_f32_e32 v227, 1.0, v226
	v_fma_f32 v227, v229, v227, v227
	v_mfma_f32_16x16x32_f16 v[218:221], v[26:29], v[170:173], v[218:221]
	v_rcp_f32_e32 v227, v227
	v_exp_f32_e32 v231, v214
	v_mfma_f32_16x16x32_f16 v[222:225], v[2:5], v[158:161], v[222:225]
	v_exp_f32_e32 v232, v215
	v_fma_f32 v226, -v226, v227, v227
	v_mfma_f32_16x16x32_f16 v[222:225], v[6:9], v[162:165], v[222:225]
	v_min_f32_e32 v233, s42, v216
	v_exp_f32_e32 v234, v217
	v_mfma_f32_16x16x32_f16 v[222:225], v[22:25], v[166:169], v[222:225]
	v_exp_f32_e32 v236, v218
	v_exp_f32_e32 v233, v233
	v_mfma_f32_16x16x32_f16 v[222:225], v[30:33], v[170:173], v[222:225]
	v_add_f32_e32 v232, 1.0, v232
	v_exp_f32_e32 v227, v219
	v_fma_f32 v235, v233, s41, s41
	v_rcp_f32_e32 v232, v232
	v_min_f32_e32 v228, s42, v220
	v_fma_f32 v235, v231, v235, v235
	v_rcp_f32_e32 v235, v235
	v_exp_f32_e32 v229, v221
	v_fma_f32 v231, -v233, v235, v235
	v_fma_f32 v201, v201, v232, v231
	v_exp_f32_e32 v228, v228
	v_min_f32_e32 v231, s42, v201
	v_exp_f32_e32 v231, v231
	v_add_f32_e32 v227, 1.0, v227
	v_add_f32_e32 v232, 1.0, v231
	v_mfma_f32_16x16x32_f16 v[146:149], v[130:133], v[158:161], v[146:149]
	v_fma_f32 v232, v234, v232, v232
	v_fma_f32 v230, v228, s41, s41
	v_rcp_f32_e32 v232, v232
	v_mfma_f32_16x16x32_f16 v[146:149], v[134:137], v[162:165], v[146:149]
	v_fma_f32 v231, -v231, v232, v232
	v_rcp_f32_e32 v227, v227
	v_cvt_pk_f16_f32 v246, v226, v231
	buffer_load_dwordx4 v[130:133], v189, s[72:75], s46 offen
	buffer_load_dwordx4 v[134:137], v208, s[72:75], s46 offen
	v_exp_f32_e32 v231, v222
	v_fma_f32 v230, v236, v230, v230
	v_exp_f32_e32 v232, v223
	s_waitcnt lgkmcnt(0)
	v_mfma_f32_16x16x32_f16 v[210:213], v[70:73], v[150:153], v[98:101]
	v_min_f32_e32 v233, s42, v224
	v_rcp_f32_e32 v230, v230
	v_exp_f32_e32 v234, v225
	v_mfma_f32_16x16x32_f16 v[214:217], v[74:77], v[150:153], v[102:105]
	v_exp_f32_e32 v233, v233
	v_fma_f32 v236, -v228, v230, v230
	v_add_f32_e32 v232, 1.0, v232
	v_fma_f32 v235, v233, s41, s41
	v_fma_f32 v198, v198, v227, v236
	v_rcp_f32_e32 v232, v232
	v_fma_f32 v235, v231, v235, v235
	v_min_f32_e32 v236, s42, v198
	v_rcp_f32_e32 v235, v235
	s_nop 0
	v_fma_f32 v231, -v233, v235, v235
	v_exp_f32_e32 v236, v236
	v_fma_f32 v199, v199, v232, v231
	v_min_f32_e32 v231, s42, v199
	v_add_f32_e32 v227, 1.0, v236
	v_exp_f32_e32 v231, v231
	v_fma_f32 v227, v229, v227, v227
	v_add_f32_e32 v232, 1.0, v231
	v_rcp_f32_e32 v227, v227
	v_fma_f32 v232, v234, v232, v232
	v_fma_f32 v236, -v236, v227, v227
	v_rcp_f32_e32 v232, v232
	s_nop 0
	v_fma_f32 v231, -v231, v232, v232
	v_cvt_pk_f16_f32 v247, v236, v231
	ds_write_b64 v250, v[246:247] offset:24576
	v_mfma_f32_16x16x32_f16 v[210:213], v[66:69], v[154:157], v[210:213]
	v_mfma_f32_16x16x32_f16 v[214:217], v[78:81], v[154:157], v[214:217]
	v_add_u32_e32 v250, 0x4000, v250
	v_add_u32_e32 v248, 0x4000, v248
	v_add_u32_e32 v249, 0x4000, v249
	s_waitcnt lgkmcnt(0)
	s_barrier
	ds_read_b128 v[158:161], v248 offset:0
	ds_read_b128 v[162:165], v248 offset:1024
	ds_read_b128 v[166:169], v249 offset:2048
	ds_read_b128 v[170:173], v249 offset:3072
	v_mfma_f32_16x16x32_f16 v[218:221], v[82:85], v[150:153], v[106:109]
	v_mfma_f32_16x16x32_f16 v[222:225], v[90:93], v[150:153], v[110:113]
	v_mfma_f32_16x16x32_f16 v[218:221], v[86:89], v[154:157], v[218:221]
	v_mfma_f32_16x16x32_f16 v[222:225], v[94:97], v[154:157], v[222:225]
	s_waitcnt lgkmcnt(2)
	v_mfma_f32_16x16x32_f16 v[210:213], v[54:57], v[158:161], v[210:213]
	v_mfma_f32_16x16x32_f16 v[210:213], v[58:61], v[162:165], v[210:213]
	s_waitcnt lgkmcnt(0)
	v_mfma_f32_16x16x32_f16 v[210:213], v[62:65], v[166:169], v[210:213]
	v_mfma_f32_16x16x32_f16 v[210:213], v[50:53], v[170:173], v[210:213]
	s_waitcnt vmcnt(7)
	v_cvt_pk_f16_f32 v251, v192, v193
	ds_write_b32 v1, v251 offset:0
	ds_read_b128 v[150:153], v186 offset:6144
	ds_read_b128 v[154:157], v186 offset:7168
	s_nop 2
	v_exp_f32_e32 v226, v210
	v_exp_f32_e32 v227, v211
	v_mfma_f32_16x16x32_f16 v[214:217], v[34:37], v[158:161], v[214:217]
	v_min_f32_e32 v228, s42, v212
	v_exp_f32_e32 v229, v213
	v_mfma_f32_16x16x32_f16 v[214:217], v[38:41], v[162:165], v[214:217]
	v_exp_f32_e32 v228, v228
	v_add_f32_e32 v227, 1.0, v227
	v_mfma_f32_16x16x32_f16 v[214:217], v[42:45], v[166:169], v[214:217]
	v_fma_f32 v230, v228, s41, s41
	v_rcp_f32_e32 v227, v227
	v_mfma_f32_16x16x32_f16 v[214:217], v[46:49], v[170:173], v[214:217]
	v_fma_f32 v230, v226, v230, v230
	v_rcp_f32_e32 v230, v230
	v_mfma_f32_16x16x32_f16 v[218:221], v[18:21], v[158:161], v[218:221]
	v_fma_f32 v226, -v228, v230, v230
	v_fma_f32 v200, v200, v227, v226
	v_mfma_f32_16x16x32_f16 v[218:221], v[14:17], v[162:165], v[218:221]
	v_min_f32_e32 v226, s42, v200
	v_exp_f32_e32 v226, v226
	v_mfma_f32_16x16x32_f16 v[218:221], v[10:13], v[166:169], v[218:221]
	v_add_f32_e32 v227, 1.0, v226
	v_fma_f32 v227, v229, v227, v227
	v_mfma_f32_16x16x32_f16 v[218:221], v[26:29], v[170:173], v[218:221]
	v_rcp_f32_e32 v227, v227
	v_exp_f32_e32 v231, v214
	v_mfma_f32_16x16x32_f16 v[222:225], v[2:5], v[158:161], v[222:225]
	v_exp_f32_e32 v232, v215
	v_fma_f32 v226, -v226, v227, v227
	v_mfma_f32_16x16x32_f16 v[222:225], v[6:9], v[162:165], v[222:225]
	v_min_f32_e32 v233, s42, v216
	v_exp_f32_e32 v234, v217
	v_mfma_f32_16x16x32_f16 v[222:225], v[22:25], v[166:169], v[222:225]
	v_exp_f32_e32 v236, v218
	v_exp_f32_e32 v233, v233
	v_mfma_f32_16x16x32_f16 v[222:225], v[30:33], v[170:173], v[222:225]
	v_add_f32_e32 v232, 1.0, v232
	v_exp_f32_e32 v227, v219
	v_fma_f32 v235, v233, s41, s41
	v_rcp_f32_e32 v232, v232
	v_min_f32_e32 v228, s42, v220
	v_fma_f32 v235, v231, v235, v235
	v_rcp_f32_e32 v235, v235
	v_exp_f32_e32 v229, v221
	v_fma_f32 v231, -v233, v235, v235
	v_fma_f32 v201, v201, v232, v231
	v_exp_f32_e32 v228, v228
	v_min_f32_e32 v231, s42, v201
	v_exp_f32_e32 v231, v231
	v_add_f32_e32 v227, 1.0, v227
	v_add_f32_e32 v232, 1.0, v231
	v_mfma_f32_16x16x32_f16 v[146:149], v[122:125], v[158:161], v[146:149]
	v_fma_f32 v232, v234, v232, v232
	v_fma_f32 v230, v228, s41, s41
	v_rcp_f32_e32 v232, v232
	v_mfma_f32_16x16x32_f16 v[146:149], v[126:129], v[162:165], v[146:149]
	v_fma_f32 v231, -v231, v232, v232
	v_rcp_f32_e32 v227, v227
	v_cvt_pk_f16_f32 v246, v226, v231
	buffer_load_dwordx4 v[122:125], v189, s[76:79], s46 offen
	buffer_load_dwordx4 v[126:129], v208, s[76:79], s46 offen
	v_exp_f32_e32 v231, v222
	v_fma_f32 v230, v236, v230, v230
	v_exp_f32_e32 v232, v223
	s_waitcnt lgkmcnt(0)
	v_mfma_f32_16x16x32_f16 v[210:213], v[70:73], v[150:153], v[98:101]
	v_min_f32_e32 v233, s42, v224
	v_rcp_f32_e32 v230, v230
	v_exp_f32_e32 v234, v225
	v_mfma_f32_16x16x32_f16 v[214:217], v[74:77], v[150:153], v[102:105]
	v_exp_f32_e32 v233, v233
	v_fma_f32 v236, -v228, v230, v230
	v_add_f32_e32 v232, 1.0, v232
	v_fma_f32 v235, v233, s41, s41
	v_fma_f32 v198, v198, v227, v236
	v_rcp_f32_e32 v232, v232
	v_fma_f32 v235, v231, v235, v235
	v_min_f32_e32 v236, s42, v198
	v_rcp_f32_e32 v235, v235
	s_nop 0
	v_fma_f32 v231, -v233, v235, v235
	v_exp_f32_e32 v236, v236
	v_fma_f32 v199, v199, v232, v231
	v_min_f32_e32 v231, s42, v199
	v_add_f32_e32 v227, 1.0, v236
	v_exp_f32_e32 v231, v231
	v_fma_f32 v227, v229, v227, v227
	v_add_f32_e32 v232, 1.0, v231
	v_rcp_f32_e32 v227, v227
	v_fma_f32 v232, v234, v232, v232
	v_fma_f32 v236, -v236, v227, v227
	v_rcp_f32_e32 v232, v232
	s_nop 0
	v_fma_f32 v231, -v231, v232, v232
	v_cvt_pk_f16_f32 v247, v236, v231
	ds_write_b64 v250, v[246:247] offset:12288
	v_mfma_f32_16x16x32_f16 v[210:213], v[66:69], v[154:157], v[210:213]
	v_mfma_f32_16x16x32_f16 v[214:217], v[78:81], v[154:157], v[214:217]
	s_waitcnt lgkmcnt(0)
	s_barrier
	ds_read_b128 v[158:161], v248 offset:4096
	ds_read_b128 v[162:165], v248 offset:5120
	ds_read_b128 v[166:169], v249 offset:6144
	ds_read_b128 v[170:173], v249 offset:7168
	v_mfma_f32_16x16x32_f16 v[218:221], v[82:85], v[150:153], v[106:109]
	v_mfma_f32_16x16x32_f16 v[222:225], v[90:93], v[150:153], v[110:113]
	v_mfma_f32_16x16x32_f16 v[218:221], v[86:89], v[154:157], v[218:221]
	v_mfma_f32_16x16x32_f16 v[222:225], v[94:97], v[154:157], v[222:225]
	s_waitcnt lgkmcnt(2)
	v_mfma_f32_16x16x32_f16 v[210:213], v[54:57], v[158:161], v[210:213]
	v_mfma_f32_16x16x32_f16 v[210:213], v[58:61], v[162:165], v[210:213]
	s_waitcnt lgkmcnt(0)
	v_mfma_f32_16x16x32_f16 v[210:213], v[62:65], v[166:169], v[210:213]
	v_mfma_f32_16x16x32_f16 v[210:213], v[50:53], v[170:173], v[210:213]
	s_waitcnt vmcnt(6)
	v_cvt_pk_f16_f32 v251, v190, v191
	ds_write_b32 v1, v251 offset:2048
	ds_read_b128 v[150:153], v186 offset:0
	ds_read_b128 v[154:157], v186 offset:1024
	s_nop 2
	v_exp_f32_e32 v226, v210
	v_exp_f32_e32 v227, v211
	v_mfma_f32_16x16x32_f16 v[214:217], v[34:37], v[158:161], v[214:217]
	v_min_f32_e32 v228, s42, v212
	v_exp_f32_e32 v229, v213
	v_mfma_f32_16x16x32_f16 v[214:217], v[38:41], v[162:165], v[214:217]
	v_exp_f32_e32 v228, v228
	v_add_f32_e32 v227, 1.0, v227
	v_mfma_f32_16x16x32_f16 v[214:217], v[42:45], v[166:169], v[214:217]
	v_fma_f32 v230, v228, s41, s41
	v_rcp_f32_e32 v227, v227
	v_mfma_f32_16x16x32_f16 v[214:217], v[46:49], v[170:173], v[214:217]
	v_fma_f32 v230, v226, v230, v230
	v_rcp_f32_e32 v230, v230
	v_mfma_f32_16x16x32_f16 v[218:221], v[18:21], v[158:161], v[218:221]
	v_fma_f32 v226, -v228, v230, v230
	v_fma_f32 v200, v200, v227, v226
	v_mfma_f32_16x16x32_f16 v[218:221], v[14:17], v[162:165], v[218:221]
	v_min_f32_e32 v226, s42, v200
	v_exp_f32_e32 v226, v226
	v_mfma_f32_16x16x32_f16 v[218:221], v[10:13], v[166:169], v[218:221]
	v_add_f32_e32 v227, 1.0, v226
	v_fma_f32 v227, v229, v227, v227
	v_mfma_f32_16x16x32_f16 v[218:221], v[26:29], v[170:173], v[218:221]
	v_rcp_f32_e32 v227, v227
	v_exp_f32_e32 v231, v214
	v_mfma_f32_16x16x32_f16 v[222:225], v[2:5], v[158:161], v[222:225]
	v_exp_f32_e32 v232, v215
	v_fma_f32 v226, -v226, v227, v227
	v_mfma_f32_16x16x32_f16 v[222:225], v[6:9], v[162:165], v[222:225]
	v_min_f32_e32 v233, s42, v216
	v_exp_f32_e32 v234, v217
	v_mfma_f32_16x16x32_f16 v[222:225], v[22:25], v[166:169], v[222:225]
	v_exp_f32_e32 v236, v218
	v_exp_f32_e32 v233, v233
	v_mfma_f32_16x16x32_f16 v[222:225], v[30:33], v[170:173], v[222:225]
	v_add_f32_e32 v232, 1.0, v232
	v_exp_f32_e32 v227, v219
	v_fma_f32 v235, v233, s41, s41
	v_rcp_f32_e32 v232, v232
	v_min_f32_e32 v228, s42, v220
	v_fma_f32 v235, v231, v235, v235
	v_rcp_f32_e32 v235, v235
	v_exp_f32_e32 v229, v221
	v_fma_f32 v231, -v233, v235, v235
	v_fma_f32 v201, v201, v232, v231
	v_exp_f32_e32 v228, v228
	v_min_f32_e32 v231, s42, v201
	v_exp_f32_e32 v231, v231
	v_add_f32_e32 v227, 1.0, v227
	v_add_f32_e32 v232, 1.0, v231
	v_mfma_f32_16x16x32_f16 v[146:149], v[114:117], v[158:161], v[146:149]
	v_fma_f32 v232, v234, v232, v232
	v_fma_f32 v230, v228, s41, s41
	v_rcp_f32_e32 v232, v232
	v_mfma_f32_16x16x32_f16 v[146:149], v[118:121], v[162:165], v[146:149]
	v_fma_f32 v231, -v231, v232, v232
	v_rcp_f32_e32 v227, v227
	v_cvt_pk_f16_f32 v246, v226, v231
	v_exp_f32_e32 v231, v222
	v_fma_f32 v230, v236, v230, v230
	v_exp_f32_e32 v232, v223
	s_waitcnt lgkmcnt(0)
	v_mfma_f32_16x16x32_f16 v[210:213], v[70:73], v[150:153], v[98:101]
	v_min_f32_e32 v233, s42, v224
	v_rcp_f32_e32 v230, v230
	v_exp_f32_e32 v234, v225
	v_mfma_f32_16x16x32_f16 v[214:217], v[74:77], v[150:153], v[102:105]
	v_exp_f32_e32 v233, v233
	v_fma_f32 v236, -v228, v230, v230
	v_add_f32_e32 v232, 1.0, v232
	v_fma_f32 v235, v233, s41, s41
	v_fma_f32 v198, v198, v227, v236
	v_rcp_f32_e32 v232, v232
	v_fma_f32 v235, v231, v235, v235
	v_min_f32_e32 v236, s42, v198
	v_rcp_f32_e32 v235, v235
	s_nop 0
	v_fma_f32 v231, -v233, v235, v235
	v_exp_f32_e32 v236, v236
	v_fma_f32 v199, v199, v232, v231
	v_min_f32_e32 v231, s42, v199
	v_add_f32_e32 v227, 1.0, v236
	v_exp_f32_e32 v231, v231
	v_fma_f32 v227, v229, v227, v227
	v_add_f32_e32 v232, 1.0, v231
	v_rcp_f32_e32 v227, v227
	v_fma_f32 v232, v234, v232, v232
	v_fma_f32 v236, -v236, v227, v227
	v_rcp_f32_e32 v232, v232
	s_nop 0
	v_fma_f32 v231, -v231, v232, v232
	v_cvt_pk_f16_f32 v247, v236, v231
	ds_write_b64 v250, v[246:247] offset:16384
	v_mfma_f32_16x16x32_f16 v[210:213], v[66:69], v[154:157], v[210:213]
	v_mfma_f32_16x16x32_f16 v[214:217], v[78:81], v[154:157], v[214:217]
	s_add_i32 s45, s45, 0x400000
	s_add_i32 s46, s46, 0x10000
	s_waitcnt lgkmcnt(0)
	s_barrier
	ds_read_b128 v[158:161], v248 offset:8192
	ds_read_b128 v[162:165], v248 offset:9216
	ds_read_b128 v[166:169], v249 offset:10240
	ds_read_b128 v[170:173], v249 offset:11264
	v_mfma_f32_16x16x32_f16 v[218:221], v[82:85], v[150:153], v[106:109]
	v_mfma_f32_16x16x32_f16 v[222:225], v[90:93], v[150:153], v[110:113]
	v_mfma_f32_16x16x32_f16 v[218:221], v[86:89], v[154:157], v[218:221]
	v_mfma_f32_16x16x32_f16 v[222:225], v[94:97], v[154:157], v[222:225]
	s_waitcnt lgkmcnt(2)
	v_mfma_f32_16x16x32_f16 v[210:213], v[54:57], v[158:161], v[210:213]
	v_mfma_f32_16x16x32_f16 v[210:213], v[58:61], v[162:165], v[210:213]
	s_waitcnt lgkmcnt(0)
	v_mfma_f32_16x16x32_f16 v[210:213], v[62:65], v[166:169], v[210:213]
	v_mfma_f32_16x16x32_f16 v[210:213], v[50:53], v[170:173], v[210:213]
	s_waitcnt vmcnt(4)
	ds_read_b128 v[150:153], v186 offset:2048
	ds_read_b128 v[154:157], v186 offset:3072
	s_nop 4
	v_exp_f32_e32 v226, v210
	v_exp_f32_e32 v227, v211
	v_mfma_f32_16x16x32_f16 v[214:217], v[34:37], v[158:161], v[214:217]
	v_min_f32_e32 v228, s42, v212
	v_exp_f32_e32 v229, v213
	v_mfma_f32_16x16x32_f16 v[214:217], v[38:41], v[162:165], v[214:217]
	v_exp_f32_e32 v228, v228
	v_add_f32_e32 v227, 1.0, v227
	v_mfma_f32_16x16x32_f16 v[214:217], v[42:45], v[166:169], v[214:217]
	v_fma_f32 v230, v228, s41, s41
	v_rcp_f32_e32 v227, v227
	v_mfma_f32_16x16x32_f16 v[214:217], v[46:49], v[170:173], v[214:217]
	v_fma_f32 v230, v226, v230, v230
	v_rcp_f32_e32 v230, v230
	v_mfma_f32_16x16x32_f16 v[218:221], v[18:21], v[158:161], v[218:221]
	v_fma_f32 v226, -v228, v230, v230
	v_fma_f32 v200, v200, v227, v226
	v_mfma_f32_16x16x32_f16 v[218:221], v[14:17], v[162:165], v[218:221]
	v_min_f32_e32 v226, s42, v200
	v_exp_f32_e32 v226, v226
	v_mfma_f32_16x16x32_f16 v[218:221], v[10:13], v[166:169], v[218:221]
	v_add_f32_e32 v227, 1.0, v226
	v_fma_f32 v227, v229, v227, v227
	v_mfma_f32_16x16x32_f16 v[218:221], v[26:29], v[170:173], v[218:221]
	v_rcp_f32_e32 v227, v227
	v_exp_f32_e32 v231, v214
	v_mfma_f32_16x16x32_f16 v[222:225], v[2:5], v[158:161], v[222:225]
	v_exp_f32_e32 v232, v215
	v_fma_f32 v226, -v226, v227, v227
	v_mfma_f32_16x16x32_f16 v[222:225], v[6:9], v[162:165], v[222:225]
	v_min_f32_e32 v233, s42, v216
	v_exp_f32_e32 v234, v217
	v_mfma_f32_16x16x32_f16 v[222:225], v[22:25], v[166:169], v[222:225]
	v_exp_f32_e32 v236, v218
	v_exp_f32_e32 v233, v233
	v_mfma_f32_16x16x32_f16 v[222:225], v[30:33], v[170:173], v[222:225]
	v_add_f32_e32 v232, 1.0, v232
	v_exp_f32_e32 v227, v219
	v_fma_f32 v235, v233, s41, s41
	v_rcp_f32_e32 v232, v232
	v_min_f32_e32 v228, s42, v220
	v_fma_f32 v235, v231, v235, v235
	v_rcp_f32_e32 v235, v235
	v_exp_f32_e32 v229, v221
	v_fma_f32 v231, -v233, v235, v235
	v_fma_f32 v201, v201, v232, v231
	v_exp_f32_e32 v228, v228
	v_min_f32_e32 v231, s42, v201
	v_exp_f32_e32 v231, v231
	v_add_f32_e32 v227, 1.0, v227
	v_add_f32_e32 v232, 1.0, v231
	v_mfma_f32_16x16x32_f16 v[146:149], v[138:141], v[158:161], v[146:149]
	v_fma_f32 v232, v234, v232, v232
	v_fma_f32 v230, v228, s41, s41
	v_rcp_f32_e32 v232, v232
	v_mfma_f32_16x16x32_f16 v[146:149], v[142:145], v[162:165], v[146:149]
	v_fma_f32 v231, -v231, v232, v232
	v_rcp_f32_e32 v227, v227
	v_cvt_pk_f16_f32 v246, v226, v231
	v_exp_f32_e32 v231, v222
	v_fma_f32 v230, v236, v230, v230
	v_exp_f32_e32 v232, v223
	s_waitcnt lgkmcnt(0)
	v_mfma_f32_16x16x32_f16 v[210:213], v[70:73], v[150:153], v[98:101]
	v_min_f32_e32 v233, s42, v224
	v_rcp_f32_e32 v230, v230
	v_exp_f32_e32 v234, v225
	v_mfma_f32_16x16x32_f16 v[214:217], v[74:77], v[150:153], v[102:105]
	v_exp_f32_e32 v233, v233
	v_fma_f32 v236, -v228, v230, v230
	v_add_f32_e32 v232, 1.0, v232
	v_fma_f32 v235, v233, s41, s41
	v_fma_f32 v198, v198, v227, v236
	v_rcp_f32_e32 v232, v232
	v_fma_f32 v235, v231, v235, v235
	v_min_f32_e32 v236, s42, v198
	v_rcp_f32_e32 v235, v235
	s_nop 0
	v_fma_f32 v231, -v233, v235, v235
	v_exp_f32_e32 v236, v236
	v_fma_f32 v199, v199, v232, v231
	v_min_f32_e32 v231, s42, v199
	v_add_f32_e32 v227, 1.0, v236
	v_exp_f32_e32 v231, v231
	v_fma_f32 v227, v229, v227, v227
	v_add_f32_e32 v232, 1.0, v231
	v_rcp_f32_e32 v227, v227
	v_fma_f32 v232, v234, v232, v232
	v_fma_f32 v236, -v236, v227, v227
	v_rcp_f32_e32 v232, v232
	s_nop 0
	v_fma_f32 v231, -v231, v232, v232
	v_cvt_pk_f16_f32 v247, v236, v231
	ds_write_b64 v250, v[246:247] offset:20480
	v_mfma_f32_16x16x32_f16 v[210:213], v[66:69], v[154:157], v[210:213]
	v_mfma_f32_16x16x32_f16 v[214:217], v[78:81], v[154:157], v[214:217]
	s_waitcnt lgkmcnt(0)
	s_barrier
	ds_read_b128 v[158:161], v248 offset:12288
	ds_read_b128 v[162:165], v248 offset:13312
	ds_read_b128 v[166:169], v249 offset:14336
	ds_read_b128 v[170:173], v249 offset:15360
	v_mfma_f32_16x16x32_f16 v[218:221], v[82:85], v[150:153], v[106:109]
	v_mfma_f32_16x16x32_f16 v[222:225], v[90:93], v[150:153], v[110:113]
	v_mfma_f32_16x16x32_f16 v[218:221], v[86:89], v[154:157], v[218:221]
	v_mfma_f32_16x16x32_f16 v[222:225], v[94:97], v[154:157], v[222:225]
	s_waitcnt lgkmcnt(2)
	v_mfma_f32_16x16x32_f16 v[210:213], v[54:57], v[158:161], v[210:213]
	v_mfma_f32_16x16x32_f16 v[210:213], v[58:61], v[162:165], v[210:213]
	s_waitcnt lgkmcnt(0)
	v_mfma_f32_16x16x32_f16 v[210:213], v[62:65], v[166:169], v[210:213]
	v_mfma_f32_16x16x32_f16 v[210:213], v[50:53], v[170:173], v[210:213]
	s_waitcnt vmcnt(2)
	s_nop 6
	v_exp_f32_e32 v226, v210
	v_exp_f32_e32 v227, v211
	v_mfma_f32_16x16x32_f16 v[214:217], v[34:37], v[158:161], v[214:217]
	v_min_f32_e32 v228, s42, v212
	v_exp_f32_e32 v229, v213
	v_mfma_f32_16x16x32_f16 v[214:217], v[38:41], v[162:165], v[214:217]
	v_exp_f32_e32 v228, v228
	v_add_f32_e32 v227, 1.0, v227
	v_mfma_f32_16x16x32_f16 v[214:217], v[42:45], v[166:169], v[214:217]
	v_fma_f32 v230, v228, s41, s41
	v_rcp_f32_e32 v227, v227
	v_mfma_f32_16x16x32_f16 v[214:217], v[46:49], v[170:173], v[214:217]
	v_fma_f32 v230, v226, v230, v230
	v_rcp_f32_e32 v230, v230
	v_mfma_f32_16x16x32_f16 v[218:221], v[18:21], v[158:161], v[218:221]
	v_fma_f32 v226, -v228, v230, v230
	v_fma_f32 v200, v200, v227, v226
	v_mfma_f32_16x16x32_f16 v[218:221], v[14:17], v[162:165], v[218:221]
	v_min_f32_e32 v226, s42, v200
	v_exp_f32_e32 v226, v226
	v_mfma_f32_16x16x32_f16 v[218:221], v[10:13], v[166:169], v[218:221]
	v_add_f32_e32 v227, 1.0, v226
	v_fma_f32 v227, v229, v227, v227
	v_mfma_f32_16x16x32_f16 v[218:221], v[26:29], v[170:173], v[218:221]
	v_rcp_f32_e32 v227, v227
	v_exp_f32_e32 v231, v214
	v_mfma_f32_16x16x32_f16 v[222:225], v[2:5], v[158:161], v[222:225]
	v_exp_f32_e32 v232, v215
	v_fma_f32 v226, -v226, v227, v227
	v_mfma_f32_16x16x32_f16 v[222:225], v[6:9], v[162:165], v[222:225]
	v_min_f32_e32 v233, s42, v216
	v_exp_f32_e32 v234, v217
	v_mfma_f32_16x16x32_f16 v[222:225], v[22:25], v[166:169], v[222:225]
	v_exp_f32_e32 v236, v218
	v_exp_f32_e32 v233, v233
	v_mfma_f32_16x16x32_f16 v[222:225], v[30:33], v[170:173], v[222:225]
	v_add_f32_e32 v232, 1.0, v232
	v_exp_f32_e32 v227, v219
	v_fma_f32 v235, v233, s41, s41
	v_rcp_f32_e32 v232, v232
	v_min_f32_e32 v228, s42, v220
	v_fma_f32 v235, v231, v235, v235
	v_rcp_f32_e32 v235, v235
	v_exp_f32_e32 v229, v221
	v_fma_f32 v231, -v233, v235, v235
	v_fma_f32 v201, v201, v232, v231
	v_exp_f32_e32 v228, v228
	v_min_f32_e32 v231, s42, v201
	v_exp_f32_e32 v231, v231
	v_add_f32_e32 v227, 1.0, v227
	v_add_f32_e32 v232, 1.0, v231
	v_mfma_f32_16x16x32_f16 v[146:149], v[130:133], v[158:161], v[146:149]
	v_fma_f32 v232, v234, v232, v232
	v_fma_f32 v230, v228, s41, s41
	v_rcp_f32_e32 v232, v232
	v_mfma_f32_16x16x32_f16 v[146:149], v[134:137], v[162:165], v[146:149]
	v_fma_f32 v231, -v231, v232, v232
	v_rcp_f32_e32 v227, v227
	v_cvt_pk_f16_f32 v246, v226, v231
	v_exp_f32_e32 v231, v222
	v_fma_f32 v230, v236, v230, v230
	v_exp_f32_e32 v232, v223
	s_waitcnt lgkmcnt(0)
	v_min_f32_e32 v233, s42, v224
	v_rcp_f32_e32 v230, v230
	v_exp_f32_e32 v234, v225
	v_exp_f32_e32 v233, v233
	v_fma_f32 v236, -v228, v230, v230
	v_add_f32_e32 v232, 1.0, v232
	v_fma_f32 v235, v233, s41, s41
	v_fma_f32 v198, v198, v227, v236
	v_rcp_f32_e32 v232, v232
	v_fma_f32 v235, v231, v235, v235
	v_min_f32_e32 v236, s42, v198
	v_rcp_f32_e32 v235, v235
	s_nop 0
	v_fma_f32 v231, -v233, v235, v235
	v_exp_f32_e32 v236, v236
	v_fma_f32 v199, v199, v232, v231
	v_min_f32_e32 v231, s42, v199
	v_add_f32_e32 v227, 1.0, v236
	v_exp_f32_e32 v231, v231
	v_fma_f32 v227, v229, v227, v227
	v_add_f32_e32 v232, 1.0, v231
	v_rcp_f32_e32 v227, v227
	v_fma_f32 v232, v234, v232, v232
	v_fma_f32 v236, -v236, v227, v227
	v_rcp_f32_e32 v232, v232
	s_nop 0
	v_fma_f32 v231, -v231, v232, v232
	v_cvt_pk_f16_f32 v247, v236, v231
	ds_write_b64 v250, v[246:247] offset:24576
	v_add_u32_e32 v250, 0x4000, v250
	v_add_u32_e32 v248, 0x4000, v248
	v_add_u32_e32 v249, 0x4000, v249
	s_waitcnt lgkmcnt(0)
	s_barrier
	s_nop 7
	ds_read_b128 v[158:161], v248 offset:0
	ds_read_b128 v[162:165], v248 offset:1024
	s_lshr_b32 s48, s35, 5
	v_and_b32_e32 v211, 15, v0
	v_bfe_u32 v212, v0, 4, 2
	v_and_b32_e32 v213, 31, v0
	v_bfe_u32 v214, v0, 5, 1
	v_add_u32_e32 v214, s48, v214
	s_lshl_b32 s49, s35, 4
	s_addk_i32 s49, 0x2000
	v_lshl_add_u32 v215, v212, 8, s49
	v_lshl_add_u32 v215, v211, 2, v215
	v_lshlrev_b32_e32 v216, 6, v213
	v_lshl_add_u32 v216, v214, 2, v216
	v_mul_u32_u24_e32 v217, 0x110, v214
	v_lshl_add_u32 v217, v213, 2, v217
	v_mul_u32_u24_e32 v218, 0x110, v211
	v_add_u32_e32 v219, 0x4000, v206
	v_add_u32_e32 v220, 0x14000, v206
	v_add_u32_e32 v221, 0x24000, v206
	v_add_u32_e32 v222, s34, v211
	v_lshlrev_b32_e32 v222, 9, v222
	v_add_u32_e32 v222, s35, v222
	v_lshl_add_u32 v222, v212, 4, v222
	s_waitcnt vmcnt(0) lgkmcnt(0)
	v_mfma_f32_16x16x32_f16 v[146:149], v[122:125], v[158:161], v[146:149]
	v_mfma_f32_16x16x32_f16 v[146:149], v[126:129], v[162:165], v[146:149]
	ds_read_b64 v[30:31], v219 offset:0
	ds_read_b64 v[32:33], v219 offset:4096
	ds_read_b64 v[34:35], v219 offset:8192
	ds_read_b64 v[36:37], v219 offset:12288
	ds_read_b64 v[38:39], v219 offset:16384
	ds_read_b64 v[40:41], v219 offset:20480
	ds_read_b64 v[42:43], v219 offset:24576
	ds_read_b64 v[44:45], v219 offset:28672
	s_waitcnt lgkmcnt(4)
	ds_read_b64 v[46:47], v219 offset:32768
	ds_read_b64 v[48:49], v219 offset:36864
	ds_read_b64 v[50:51], v219 offset:40960
	ds_read_b64 v[52:53], v219 offset:45056
	ds_read_b64 v[54:55], v219 offset:49152
	ds_read_b64 v[56:57], v219 offset:53248
	ds_read_b64 v[58:59], v219 offset:57344
	ds_read_b64 v[60:61], v219 offset:61440
	s_waitcnt lgkmcnt(4)
	ds_read_b64 v[62:63], v220 offset:0
	ds_read_b64 v[64:65], v220 offset:4096
	ds_read_b64 v[66:67], v220 offset:8192
	ds_read_b64 v[68:69], v220 offset:12288
	ds_read_b64 v[70:71], v220 offset:16384
	ds_read_b64 v[72:73], v220 offset:20480
	ds_read_b64 v[74:75], v220 offset:24576
	ds_read_b64 v[76:77], v220 offset:28672
	s_waitcnt lgkmcnt(4)
	ds_read_b64 v[78:79], v220 offset:32768
	ds_read_b64 v[80:81], v220 offset:36864
	ds_read_b64 v[82:83], v220 offset:40960
	ds_read_b64 v[84:85], v220 offset:45056
	ds_read_b64 v[86:87], v220 offset:49152
	ds_read_b64 v[88:89], v220 offset:53248
	ds_read_b64 v[90:91], v220 offset:57344
	ds_read_b64 v[92:93], v220 offset:61440
	s_waitcnt lgkmcnt(4)
	ds_read_b64 v[94:95], v221 offset:0
	ds_read_b64 v[96:97], v221 offset:4096
	ds_read_b64 v[98:99], v221 offset:8192
	ds_read_b64 v[100:101], v221 offset:12288
	ds_write2_b32 v215, v146, v147 offset1:16
	ds_write2_b32 v215, v148, v149 offset0:32 offset1:48
	s_waitcnt lgkmcnt(0)
	s_barrier
	ds_read2st64_b32 v[230:231], v216 offset0:32 offset1:48
	ds_read2st64_b32 v[232:233], v216 offset0:40 offset1:56
	v_cmp_gt_u32_e32 vcc, 18, v213
	s_waitcnt vmcnt(0) lgkmcnt(0)
	v_add_f32_e32 v223, v230, v231
	v_add_f32_e32 v224, v232, v233
	v_add_f32_e32 v223, v223, v254
	v_add_f32_e32 v224, v224, v255
	v_max_f32_e32 v223, 0, v223
	v_max_f32_e32 v224, 0, v224
	v_mov_b32_e32 v226, 0xf149f2ca
	v_cndmask_b32_e32 v224, v226, v224, vcc
	v_max_f32_e32 v225, v223, v224
	s_nop 1
	v_max_f32_dpp v226, v225, v225 quad_perm:[1,0,3,2] row_mask:0xf bank_mask:0xf
	s_nop 1
	v_max_f32_dpp v225, v226, v226 quad_perm:[2,3,0,1] row_mask:0xf bank_mask:0xf
	s_nop 1
	v_max_f32_dpp v226, v225, v225 row_half_mirror row_mask:0xf bank_mask:0xf
	s_nop 1
	v_max_f32_dpp v225, v226, v226 row_mirror row_mask:0xf bank_mask:0xf
	ds_swizzle_b32 v226, v225 offset:swizzle(SWAP,16)
	s_waitcnt lgkmcnt(0)
	v_max_f32_e32 v225, v225, v226
	v_sub_f32_e32 v223, v223, v225
	v_sub_f32_e32 v224, v224, v225
	v_mul_f32_e32 v223, 0x3fb8aa3b, v223
	v_mul_f32_e32 v224, 0x3fb8aa3b, v224
	v_exp_f32_e32 v227, v223
	v_exp_f32_e32 v228, v224
	s_nop 0
	v_add_f32_e32 v229, v227, v228
	s_nop 1
	v_add_f32_dpp v226, v229, v229 quad_perm:[1,0,3,2] row_mask:0xf bank_mask:0xf
	s_nop 1
	v_add_f32_dpp v229, v226, v226 quad_perm:[2,3,0,1] row_mask:0xf bank_mask:0xf
	s_nop 1
	v_add_f32_dpp v226, v229, v229 row_half_mirror row_mask:0xf bank_mask:0xf
	s_nop 1
	v_add_f32_dpp v229, v226, v226 row_mirror row_mask:0xf bank_mask:0xf
	ds_swizzle_b32 v226, v229 offset:swizzle(SWAP,16)
	s_waitcnt lgkmcnt(0)
	v_add_f32_e32 v229, v229, v226
	v_rcp_f32_e32 v234, v229
	s_nop 0
	v_mul_f32_e32 v227, v227, v234
	v_mul_f32_e32 v228, v228, v234
	ds_write_b32 v217, v227
	ds_write_b32 v217, v228 offset:128
	s_waitcnt lgkmcnt(0)
	s_barrier
	ds_read_b128 v[102:105], v218 offset:0
	ds_read_b128 v[106:109], v218 offset:16
	ds_read_b128 v[110:113], v218 offset:32
	ds_read_b128 v[114:117], v218 offset:48
	ds_read_b128 v[118:121], v218 offset:64
	ds_read_b128 v[122:125], v218 offset:80
	ds_read_b128 v[126:129], v218 offset:96
	ds_read_b128 v[130:133], v218 offset:112
	ds_read_b128 v[134:137], v218 offset:128
	ds_read_b128 v[138:141], v218 offset:144
	ds_read_b128 v[142:145], v218 offset:160
	ds_read_b128 v[146:149], v218 offset:176
	ds_read_b128 v[150:153], v218 offset:192
	v_mov_b32_e32 v154, 0
	v_mov_b32_e32 v155, 0
	v_mov_b32_e32 v156, 0
	v_mov_b32_e32 v157, 0
	s_waitcnt vmcnt(0) lgkmcnt(0)
	v_fma_mix_f32 v154, v174, v102, v154 op_sel_hi:[1,0,0]
	v_fma_mix_f32 v155, v174, v102, v155 op_sel:[1,0,0] op_sel_hi:[1,0,0]
	v_fma_mix_f32 v156, v175, v102, v156 op_sel_hi:[1,0,0]
	v_fma_mix_f32 v157, v175, v102, v157 op_sel:[1,0,0] op_sel_hi:[1,0,0]
	v_fma_mix_f32 v154, v176, v103, v154 op_sel_hi:[1,0,0]
	v_fma_mix_f32 v155, v176, v103, v155 op_sel:[1,0,0] op_sel_hi:[1,0,0]
	v_fma_mix_f32 v156, v177, v103, v156 op_sel_hi:[1,0,0]
	v_fma_mix_f32 v157, v177, v103, v157 op_sel:[1,0,0] op_sel_hi:[1,0,0]
	v_fma_mix_f32 v154, v178, v104, v154 op_sel_hi:[1,0,0]
	v_fma_mix_f32 v155, v178, v104, v155 op_sel:[1,0,0] op_sel_hi:[1,0,0]
	v_fma_mix_f32 v156, v179, v104, v156 op_sel_hi:[1,0,0]
	v_fma_mix_f32 v157, v179, v104, v157 op_sel:[1,0,0] op_sel_hi:[1,0,0]
	v_fma_mix_f32 v154, v180, v105, v154 op_sel_hi:[1,0,0]
	v_fma_mix_f32 v155, v180, v105, v155 op_sel:[1,0,0] op_sel_hi:[1,0,0]
	v_fma_mix_f32 v156, v181, v105, v156 op_sel_hi:[1,0,0]
	v_fma_mix_f32 v157, v181, v105, v157 op_sel:[1,0,0] op_sel_hi:[1,0,0]
	v_fma_mix_f32 v154, v182, v106, v154 op_sel_hi:[1,0,0]
	v_fma_mix_f32 v155, v182, v106, v155 op_sel:[1,0,0] op_sel_hi:[1,0,0]
	v_fma_mix_f32 v156, v183, v106, v156 op_sel_hi:[1,0,0]
	v_fma_mix_f32 v157, v183, v106, v157 op_sel:[1,0,0] op_sel_hi:[1,0,0]
	v_fma_mix_f32 v154, v184, v107, v154 op_sel_hi:[1,0,0]
	v_fma_mix_f32 v155, v184, v107, v155 op_sel:[1,0,0] op_sel_hi:[1,0,0]
	v_fma_mix_f32 v156, v185, v107, v156 op_sel_hi:[1,0,0]
	v_fma_mix_f32 v157, v185, v107, v157 op_sel:[1,0,0] op_sel_hi:[1,0,0]
	v_fma_mix_f32 v154, v237, v108, v154 op_sel_hi:[1,0,0]
	v_fma_mix_f32 v155, v237, v108, v155 op_sel:[1,0,0] op_sel_hi:[1,0,0]
	v_fma_mix_f32 v156, v238, v108, v156 op_sel_hi:[1,0,0]
	v_fma_mix_f32 v157, v238, v108, v157 op_sel:[1,0,0] op_sel_hi:[1,0,0]
	v_fma_mix_f32 v154, v239, v109, v154 op_sel_hi:[1,0,0]
	v_fma_mix_f32 v155, v239, v109, v155 op_sel:[1,0,0] op_sel_hi:[1,0,0]
	v_fma_mix_f32 v156, v240, v109, v156 op_sel_hi:[1,0,0]
	v_fma_mix_f32 v157, v240, v109, v157 op_sel:[1,0,0] op_sel_hi:[1,0,0]
	v_fma_mix_f32 v154, v241, v110, v154 op_sel_hi:[1,0,0]
	v_fma_mix_f32 v155, v241, v110, v155 op_sel:[1,0,0] op_sel_hi:[1,0,0]
	v_fma_mix_f32 v156, v242, v110, v156 op_sel_hi:[1,0,0]
	v_fma_mix_f32 v157, v242, v110, v157 op_sel:[1,0,0] op_sel_hi:[1,0,0]
	v_fma_mix_f32 v154, v243, v111, v154 op_sel_hi:[1,0,0]
	v_fma_mix_f32 v155, v243, v111, v155 op_sel:[1,0,0] op_sel_hi:[1,0,0]
	v_fma_mix_f32 v156, v244, v111, v156 op_sel_hi:[1,0,0]
	v_fma_mix_f32 v157, v244, v111, v157 op_sel:[1,0,0] op_sel_hi:[1,0,0]
	v_fma_mix_f32 v154, v245, v112, v154 op_sel_hi:[1,0,0]
	v_fma_mix_f32 v155, v245, v112, v155 op_sel:[1,0,0] op_sel_hi:[1,0,0]
	v_fma_mix_f32 v156, v187, v112, v156 op_sel_hi:[1,0,0]
	v_fma_mix_f32 v157, v187, v112, v157 op_sel:[1,0,0] op_sel_hi:[1,0,0]
	v_fma_mix_f32 v154, v188, v113, v154 op_sel_hi:[1,0,0]
	v_fma_mix_f32 v155, v188, v113, v155 op_sel:[1,0,0] op_sel_hi:[1,0,0]
	v_fma_mix_f32 v156, v202, v113, v156 op_sel_hi:[1,0,0]
	v_fma_mix_f32 v157, v202, v113, v157 op_sel:[1,0,0] op_sel_hi:[1,0,0]
	v_fma_mix_f32 v154, v203, v114, v154 op_sel_hi:[1,0,0]
	v_fma_mix_f32 v155, v203, v114, v155 op_sel:[1,0,0] op_sel_hi:[1,0,0]
	v_fma_mix_f32 v156, v204, v114, v156 op_sel_hi:[1,0,0]
	v_fma_mix_f32 v157, v204, v114, v157 op_sel:[1,0,0] op_sel_hi:[1,0,0]
	v_fma_mix_f32 v154, v205, v115, v154 op_sel_hi:[1,0,0]
	v_fma_mix_f32 v155, v205, v115, v155 op_sel:[1,0,0] op_sel_hi:[1,0,0]
	v_fma_mix_f32 v156, v207, v115, v156 op_sel_hi:[1,0,0]
	v_fma_mix_f32 v157, v207, v115, v157 op_sel:[1,0,0] op_sel_hi:[1,0,0]
	v_fma_mix_f32 v154, v30, v116, v154 op_sel_hi:[1,0,0]
	v_fma_mix_f32 v155, v30, v116, v155 op_sel:[1,0,0] op_sel_hi:[1,0,0]
	v_fma_mix_f32 v156, v31, v116, v156 op_sel_hi:[1,0,0]
	v_fma_mix_f32 v157, v31, v116, v157 op_sel:[1,0,0] op_sel_hi:[1,0,0]
	v_fma_mix_f32 v154, v32, v117, v154 op_sel_hi:[1,0,0]
	v_fma_mix_f32 v155, v32, v117, v155 op_sel:[1,0,0] op_sel_hi:[1,0,0]
	v_fma_mix_f32 v156, v33, v117, v156 op_sel_hi:[1,0,0]
	v_fma_mix_f32 v157, v33, v117, v157 op_sel:[1,0,0] op_sel_hi:[1,0,0]
	v_fma_mix_f32 v154, v34, v118, v154 op_sel_hi:[1,0,0]
	v_fma_mix_f32 v155, v34, v118, v155 op_sel:[1,0,0] op_sel_hi:[1,0,0]
	v_fma_mix_f32 v156, v35, v118, v156 op_sel_hi:[1,0,0]
	v_fma_mix_f32 v157, v35, v118, v157 op_sel:[1,0,0] op_sel_hi:[1,0,0]
	v_fma_mix_f32 v154, v36, v119, v154 op_sel_hi:[1,0,0]
	v_fma_mix_f32 v155, v36, v119, v155 op_sel:[1,0,0] op_sel_hi:[1,0,0]
	v_fma_mix_f32 v156, v37, v119, v156 op_sel_hi:[1,0,0]
	v_fma_mix_f32 v157, v37, v119, v157 op_sel:[1,0,0] op_sel_hi:[1,0,0]
	v_fma_mix_f32 v154, v38, v120, v154 op_sel_hi:[1,0,0]
	v_fma_mix_f32 v155, v38, v120, v155 op_sel:[1,0,0] op_sel_hi:[1,0,0]
	v_fma_mix_f32 v156, v39, v120, v156 op_sel_hi:[1,0,0]
	v_fma_mix_f32 v157, v39, v120, v157 op_sel:[1,0,0] op_sel_hi:[1,0,0]
	v_fma_mix_f32 v154, v40, v121, v154 op_sel_hi:[1,0,0]
	v_fma_mix_f32 v155, v40, v121, v155 op_sel:[1,0,0] op_sel_hi:[1,0,0]
	v_fma_mix_f32 v156, v41, v121, v156 op_sel_hi:[1,0,0]
	v_fma_mix_f32 v157, v41, v121, v157 op_sel:[1,0,0] op_sel_hi:[1,0,0]
	v_fma_mix_f32 v154, v42, v122, v154 op_sel_hi:[1,0,0]
	v_fma_mix_f32 v155, v42, v122, v155 op_sel:[1,0,0] op_sel_hi:[1,0,0]
	v_fma_mix_f32 v156, v43, v122, v156 op_sel_hi:[1,0,0]
	v_fma_mix_f32 v157, v43, v122, v157 op_sel:[1,0,0] op_sel_hi:[1,0,0]
	v_fma_mix_f32 v154, v44, v123, v154 op_sel_hi:[1,0,0]
	v_fma_mix_f32 v155, v44, v123, v155 op_sel:[1,0,0] op_sel_hi:[1,0,0]
	v_fma_mix_f32 v156, v45, v123, v156 op_sel_hi:[1,0,0]
	v_fma_mix_f32 v157, v45, v123, v157 op_sel:[1,0,0] op_sel_hi:[1,0,0]
	v_fma_mix_f32 v154, v46, v124, v154 op_sel_hi:[1,0,0]
	v_fma_mix_f32 v155, v46, v124, v155 op_sel:[1,0,0] op_sel_hi:[1,0,0]
	v_fma_mix_f32 v156, v47, v124, v156 op_sel_hi:[1,0,0]
	v_fma_mix_f32 v157, v47, v124, v157 op_sel:[1,0,0] op_sel_hi:[1,0,0]
	v_fma_mix_f32 v154, v48, v125, v154 op_sel_hi:[1,0,0]
	v_fma_mix_f32 v155, v48, v125, v155 op_sel:[1,0,0] op_sel_hi:[1,0,0]
	v_fma_mix_f32 v156, v49, v125, v156 op_sel_hi:[1,0,0]
	v_fma_mix_f32 v157, v49, v125, v157 op_sel:[1,0,0] op_sel_hi:[1,0,0]
	v_fma_mix_f32 v154, v50, v126, v154 op_sel_hi:[1,0,0]
	v_fma_mix_f32 v155, v50, v126, v155 op_sel:[1,0,0] op_sel_hi:[1,0,0]
	v_fma_mix_f32 v156, v51, v126, v156 op_sel_hi:[1,0,0]
	v_fma_mix_f32 v157, v51, v126, v157 op_sel:[1,0,0] op_sel_hi:[1,0,0]
	v_fma_mix_f32 v154, v52, v127, v154 op_sel_hi:[1,0,0]
	v_fma_mix_f32 v155, v52, v127, v155 op_sel:[1,0,0] op_sel_hi:[1,0,0]
	v_fma_mix_f32 v156, v53, v127, v156 op_sel_hi:[1,0,0]
	v_fma_mix_f32 v157, v53, v127, v157 op_sel:[1,0,0] op_sel_hi:[1,0,0]
	v_fma_mix_f32 v154, v54, v128, v154 op_sel_hi:[1,0,0]
	v_fma_mix_f32 v155, v54, v128, v155 op_sel:[1,0,0] op_sel_hi:[1,0,0]
	v_fma_mix_f32 v156, v55, v128, v156 op_sel_hi:[1,0,0]
	v_fma_mix_f32 v157, v55, v128, v157 op_sel:[1,0,0] op_sel_hi:[1,0,0]
	v_fma_mix_f32 v154, v56, v129, v154 op_sel_hi:[1,0,0]
	v_fma_mix_f32 v155, v56, v129, v155 op_sel:[1,0,0] op_sel_hi:[1,0,0]
	v_fma_mix_f32 v156, v57, v129, v156 op_sel_hi:[1,0,0]
	v_fma_mix_f32 v157, v57, v129, v157 op_sel:[1,0,0] op_sel_hi:[1,0,0]
	v_fma_mix_f32 v154, v58, v130, v154 op_sel_hi:[1,0,0]
	v_fma_mix_f32 v155, v58, v130, v155 op_sel:[1,0,0] op_sel_hi:[1,0,0]
	v_fma_mix_f32 v156, v59, v130, v156 op_sel_hi:[1,0,0]
	v_fma_mix_f32 v157, v59, v130, v157 op_sel:[1,0,0] op_sel_hi:[1,0,0]
	v_fma_mix_f32 v154, v60, v131, v154 op_sel_hi:[1,0,0]
	v_fma_mix_f32 v155, v60, v131, v155 op_sel:[1,0,0] op_sel_hi:[1,0,0]
	v_fma_mix_f32 v156, v61, v131, v156 op_sel_hi:[1,0,0]
	v_fma_mix_f32 v157, v61, v131, v157 op_sel:[1,0,0] op_sel_hi:[1,0,0]
	v_fma_mix_f32 v154, v62, v132, v154 op_sel_hi:[1,0,0]
	v_fma_mix_f32 v155, v62, v132, v155 op_sel:[1,0,0] op_sel_hi:[1,0,0]
	v_fma_mix_f32 v156, v63, v132, v156 op_sel_hi:[1,0,0]
	v_fma_mix_f32 v157, v63, v132, v157 op_sel:[1,0,0] op_sel_hi:[1,0,0]
	v_fma_mix_f32 v154, v64, v133, v154 op_sel_hi:[1,0,0]
	v_fma_mix_f32 v155, v64, v133, v155 op_sel:[1,0,0] op_sel_hi:[1,0,0]
	v_fma_mix_f32 v156, v65, v133, v156 op_sel_hi:[1,0,0]
	v_fma_mix_f32 v157, v65, v133, v157 op_sel:[1,0,0] op_sel_hi:[1,0,0]
	v_fma_mix_f32 v154, v66, v134, v154 op_sel_hi:[1,0,0]
	v_fma_mix_f32 v155, v66, v134, v155 op_sel:[1,0,0] op_sel_hi:[1,0,0]
	v_fma_mix_f32 v156, v67, v134, v156 op_sel_hi:[1,0,0]
	v_fma_mix_f32 v157, v67, v134, v157 op_sel:[1,0,0] op_sel_hi:[1,0,0]
	v_fma_mix_f32 v154, v68, v135, v154 op_sel_hi:[1,0,0]
	v_fma_mix_f32 v155, v68, v135, v155 op_sel:[1,0,0] op_sel_hi:[1,0,0]
	v_fma_mix_f32 v156, v69, v135, v156 op_sel_hi:[1,0,0]
	v_fma_mix_f32 v157, v69, v135, v157 op_sel:[1,0,0] op_sel_hi:[1,0,0]
	v_fma_mix_f32 v154, v70, v136, v154 op_sel_hi:[1,0,0]
	v_fma_mix_f32 v155, v70, v136, v155 op_sel:[1,0,0] op_sel_hi:[1,0,0]
	v_fma_mix_f32 v156, v71, v136, v156 op_sel_hi:[1,0,0]
	v_fma_mix_f32 v157, v71, v136, v157 op_sel:[1,0,0] op_sel_hi:[1,0,0]
	v_fma_mix_f32 v154, v72, v137, v154 op_sel_hi:[1,0,0]
	v_fma_mix_f32 v155, v72, v137, v155 op_sel:[1,0,0] op_sel_hi:[1,0,0]
	v_fma_mix_f32 v156, v73, v137, v156 op_sel_hi:[1,0,0]
	v_fma_mix_f32 v157, v73, v137, v157 op_sel:[1,0,0] op_sel_hi:[1,0,0]
	v_fma_mix_f32 v154, v74, v138, v154 op_sel_hi:[1,0,0]
	v_fma_mix_f32 v155, v74, v138, v155 op_sel:[1,0,0] op_sel_hi:[1,0,0]
	v_fma_mix_f32 v156, v75, v138, v156 op_sel_hi:[1,0,0]
	v_fma_mix_f32 v157, v75, v138, v157 op_sel:[1,0,0] op_sel_hi:[1,0,0]
	v_fma_mix_f32 v154, v76, v139, v154 op_sel_hi:[1,0,0]
	v_fma_mix_f32 v155, v76, v139, v155 op_sel:[1,0,0] op_sel_hi:[1,0,0]
	v_fma_mix_f32 v156, v77, v139, v156 op_sel_hi:[1,0,0]
	v_fma_mix_f32 v157, v77, v139, v157 op_sel:[1,0,0] op_sel_hi:[1,0,0]
	v_fma_mix_f32 v154, v78, v140, v154 op_sel_hi:[1,0,0]
	v_fma_mix_f32 v155, v78, v140, v155 op_sel:[1,0,0] op_sel_hi:[1,0,0]
	v_fma_mix_f32 v156, v79, v140, v156 op_sel_hi:[1,0,0]
	v_fma_mix_f32 v157, v79, v140, v157 op_sel:[1,0,0] op_sel_hi:[1,0,0]
	v_fma_mix_f32 v154, v80, v141, v154 op_sel_hi:[1,0,0]
	v_fma_mix_f32 v155, v80, v141, v155 op_sel:[1,0,0] op_sel_hi:[1,0,0]
	v_fma_mix_f32 v156, v81, v141, v156 op_sel_hi:[1,0,0]
	v_fma_mix_f32 v157, v81, v141, v157 op_sel:[1,0,0] op_sel_hi:[1,0,0]
	v_fma_mix_f32 v154, v82, v142, v154 op_sel_hi:[1,0,0]
	v_fma_mix_f32 v155, v82, v142, v155 op_sel:[1,0,0] op_sel_hi:[1,0,0]
	v_fma_mix_f32 v156, v83, v142, v156 op_sel_hi:[1,0,0]
	v_fma_mix_f32 v157, v83, v142, v157 op_sel:[1,0,0] op_sel_hi:[1,0,0]
	v_fma_mix_f32 v154, v84, v143, v154 op_sel_hi:[1,0,0]
	v_fma_mix_f32 v155, v84, v143, v155 op_sel:[1,0,0] op_sel_hi:[1,0,0]
	v_fma_mix_f32 v156, v85, v143, v156 op_sel_hi:[1,0,0]
	v_fma_mix_f32 v157, v85, v143, v157 op_sel:[1,0,0] op_sel_hi:[1,0,0]
	v_fma_mix_f32 v154, v86, v144, v154 op_sel_hi:[1,0,0]
	v_fma_mix_f32 v155, v86, v144, v155 op_sel:[1,0,0] op_sel_hi:[1,0,0]
	v_fma_mix_f32 v156, v87, v144, v156 op_sel_hi:[1,0,0]
	v_fma_mix_f32 v157, v87, v144, v157 op_sel:[1,0,0] op_sel_hi:[1,0,0]
	v_fma_mix_f32 v154, v88, v145, v154 op_sel_hi:[1,0,0]
	v_fma_mix_f32 v155, v88, v145, v155 op_sel:[1,0,0] op_sel_hi:[1,0,0]
	v_fma_mix_f32 v156, v89, v145, v156 op_sel_hi:[1,0,0]
	v_fma_mix_f32 v157, v89, v145, v157 op_sel:[1,0,0] op_sel_hi:[1,0,0]
	v_fma_mix_f32 v154, v90, v146, v154 op_sel_hi:[1,0,0]
	v_fma_mix_f32 v155, v90, v146, v155 op_sel:[1,0,0] op_sel_hi:[1,0,0]
	v_fma_mix_f32 v156, v91, v146, v156 op_sel_hi:[1,0,0]
	v_fma_mix_f32 v157, v91, v146, v157 op_sel:[1,0,0] op_sel_hi:[1,0,0]
	v_fma_mix_f32 v154, v92, v147, v154 op_sel_hi:[1,0,0]
	v_fma_mix_f32 v155, v92, v147, v155 op_sel:[1,0,0] op_sel_hi:[1,0,0]
	v_fma_mix_f32 v156, v93, v147, v156 op_sel_hi:[1,0,0]
	v_fma_mix_f32 v157, v93, v147, v157 op_sel:[1,0,0] op_sel_hi:[1,0,0]
	v_fma_mix_f32 v154, v94, v148, v154 op_sel_hi:[1,0,0]
	v_fma_mix_f32 v155, v94, v148, v155 op_sel:[1,0,0] op_sel_hi:[1,0,0]
	v_fma_mix_f32 v156, v95, v148, v156 op_sel_hi:[1,0,0]
	v_fma_mix_f32 v157, v95, v148, v157 op_sel:[1,0,0] op_sel_hi:[1,0,0]
	v_fma_mix_f32 v154, v96, v149, v154 op_sel_hi:[1,0,0]
	v_fma_mix_f32 v155, v96, v149, v155 op_sel:[1,0,0] op_sel_hi:[1,0,0]
	v_fma_mix_f32 v156, v97, v149, v156 op_sel_hi:[1,0,0]
	v_fma_mix_f32 v157, v97, v149, v157 op_sel:[1,0,0] op_sel_hi:[1,0,0]
	v_fma_mix_f32 v154, v98, v150, v154 op_sel_hi:[1,0,0]
	v_fma_mix_f32 v155, v98, v150, v155 op_sel:[1,0,0] op_sel_hi:[1,0,0]
	v_fma_mix_f32 v156, v99, v150, v156 op_sel_hi:[1,0,0]
	v_fma_mix_f32 v157, v99, v150, v157 op_sel:[1,0,0] op_sel_hi:[1,0,0]
	v_fma_mix_f32 v154, v100, v151, v154 op_sel_hi:[1,0,0]
	v_fma_mix_f32 v155, v100, v151, v155 op_sel:[1,0,0] op_sel_hi:[1,0,0]
	v_fma_mix_f32 v156, v101, v151, v156 op_sel_hi:[1,0,0]
	v_fma_mix_f32 v157, v101, v151, v157 op_sel:[1,0,0] op_sel_hi:[1,0,0]
	global_store_dwordx4 v222, v[154:157], s[8:9]
	s_endpgm
